# PEER top-k score stage rescheduled: subkey fragments requested up front, query fragments streamed, independent accumulators (on top of v36)
# baseline (speedup 1.0000x reference)
.LBB0_977:
	s_or_b64 exec, exec, s[18:19]
	s_lshl_b32 s18, s28, 16
	v_readlane_b32 s19, v255, 18
	v_and_b32_e32 v10, 15, v2
	s_or_b32 s18, s18, s19
	v_readlane_b32 s19, v255, 4
	v_or_b32_e32 v0, s61, v10
	s_add_u32 s18, s19, s18
	v_readlane_b32 s19, v255, 12
	v_ashrrev_i32_e32 v1, 31, v0
	s_addc_u32 s19, s19, 0
	v_lshlrev_b64 v[0:1], 8, v[0:1]
	v_lshl_add_u64 v[0:1], s[18:19], 0, v[0:1]
	v_and_b32_e32 v104, 48, v2
	v_and_b32_e32 v20, 63, v2
	v_lshl_add_u64 v[0:1], v[0:1], 0, v[104:105]
	v_lshrrev_b32_e32 v2, 2, v2
	s_waitcnt lgkmcnt(0)
	s_barrier
	v_and_b32_e32 v11, 12, v2
	global_load_dwordx4 v[112:115], v[0:1], off
	global_load_dwordx4 v[116:119], v[0:1], off offset:64
	global_load_dwordx4 v[120:123], v[0:1], off offset:128
	global_load_dwordx4 v[124:127], v[0:1], off offset:192
	s_mov_b32 s19, 0x8000
	v_add_co_u32_e32 v24, vcc, s19, v0
	v_lshl_add_u32 v23, v10, 2, v16
	v_mul_u32_u24_e32 v10, 0x210, v10
	v_addc_co_u32_e32 v25, vcc, 0, v1, vcc
	v_add3_u32 v21, v12, v104, v10
	global_load_dwordx4 v[128:131], v[24:25], off
	global_load_dwordx4 v[132:135], v[24:25], off offset:64
	global_load_dwordx4 v[136:139], v[24:25], off offset:128
	global_load_dwordx4 v[140:143], v[24:25], off offset:192
	ds_read_b128 v[58:61], v21
	ds_read_b128 v[62:65], v21 offset:64
	ds_read_b128 v[66:69], v21 offset:128
	ds_read_b128 v[70:73], v21 offset:192
	ds_read_b128 v[74:77], v21 offset:8448
	ds_read_b128 v[78:81], v21 offset:8512
	ds_read_b128 v[82:85], v21 offset:8576
	ds_read_b128 v[86:89], v21 offset:8640
	ds_read_b128 v[90:93], v21 offset:16896
	ds_read_b128 v[94:97], v21 offset:16960
	ds_read_b128 v[98:101], v21 offset:17024
	ds_read_b128 v[146:149], v21 offset:17088
	s_movk_i32 s18, 0x404
	v_mad_u32_u24 v22, v11, s18, v23
	v_add_u32_e32 v110, 0x8400, v22
	s_waitcnt vmcnt(4) lgkmcnt(8)
	v_mfma_f32_16x16x32_bf16 v[166:169], v[58:61], v[112:115], 0
	v_mfma_f32_16x16x32_bf16 v[166:169], v[62:65], v[116:119], v[166:169]
	v_mfma_f32_16x16x32_bf16 v[166:169], v[66:69], v[120:123], v[166:169]
	v_mfma_f32_16x16x32_bf16 v[166:169], v[70:73], v[124:127], v[166:169]
	ds_read_b128 v[150:153], v21 offset:25344
	ds_read_b128 v[154:157], v21 offset:25408
	ds_read_b128 v[158:161], v21 offset:25472
	ds_read_b128 v[162:165], v21 offset:25536
	s_waitcnt lgkmcnt(8)
	v_mfma_f32_16x16x32_bf16 v[170:173], v[74:77], v[112:115], 0
	v_mfma_f32_16x16x32_bf16 v[170:173], v[78:81], v[116:119], v[170:173]
	v_mfma_f32_16x16x32_bf16 v[170:173], v[82:85], v[120:123], v[170:173]
	v_mfma_f32_16x16x32_bf16 v[170:173], v[86:89], v[124:127], v[170:173]
	s_waitcnt lgkmcnt(4)
	v_mfma_f32_16x16x32_bf16 v[174:177], v[90:93], v[112:115], 0
	v_mfma_f32_16x16x32_bf16 v[174:177], v[94:97], v[116:119], v[174:177]
	v_mfma_f32_16x16x32_bf16 v[174:177], v[98:101], v[120:123], v[174:177]
	v_mfma_f32_16x16x32_bf16 v[174:177], v[146:149], v[124:127], v[174:177]
	s_waitcnt lgkmcnt(0)
	v_mfma_f32_16x16x32_bf16 v[178:181], v[150:153], v[112:115], 0
	v_mfma_f32_16x16x32_bf16 v[178:181], v[154:157], v[116:119], v[178:181]
	v_mfma_f32_16x16x32_bf16 v[178:181], v[158:161], v[120:123], v[178:181]
	v_mfma_f32_16x16x32_bf16 v[178:181], v[162:165], v[124:127], v[178:181]
	ds_read_b128 v[58:61], v21 offset:256
	ds_read_b128 v[62:65], v21 offset:320
	ds_read_b128 v[66:69], v21 offset:384
	ds_read_b128 v[70:73], v21 offset:448
	ds_read_b128 v[74:77], v21 offset:8704
	ds_read_b128 v[78:81], v21 offset:8768
	ds_read_b128 v[82:85], v21 offset:8832
	ds_read_b128 v[86:89], v21 offset:8896
	ds_write_b32 v110, v166 offset:0
	ds_write_b32 v110, v167 offset:1028
	ds_write_b32 v110, v168 offset:2056
	ds_write_b32 v110, v169 offset:3084
	ds_write_b32 v110, v170 offset:16448
	ds_write_b32 v110, v171 offset:17476
	ds_write_b32 v110, v172 offset:18504
	s_waitcnt lgkmcnt(14)
	ds_write_b32 v110, v173 offset:19532
	s_waitcnt lgkmcnt(14)
	ds_read_b128 v[90:93], v21 offset:17152
	s_waitcnt lgkmcnt(14)
	ds_read_b128 v[94:97], v21 offset:17216
	s_waitcnt lgkmcnt(14)
	ds_read_b128 v[98:101], v21 offset:17280
	s_waitcnt lgkmcnt(14)
	ds_read_b128 v[146:149], v21 offset:17344
	s_waitcnt lgkmcnt(14)
	ds_write_b32 v110, v174 offset:32896
	s_waitcnt lgkmcnt(14)
	ds_write_b32 v110, v175 offset:33924
	s_waitcnt lgkmcnt(14)
	ds_write_b32 v110, v176 offset:34952
	s_waitcnt lgkmcnt(14)
	ds_write_b32 v110, v177 offset:35980
	s_nop 3
	s_waitcnt lgkmcnt(14)
	ds_write_b32 v110, v178 offset:49344
	s_waitcnt lgkmcnt(14)
	ds_write_b32 v110, v179 offset:50372
	s_waitcnt lgkmcnt(14)
	ds_write_b32 v110, v180 offset:51400
	s_waitcnt lgkmcnt(14)
	ds_write_b32 v110, v181 offset:52428
	s_waitcnt vmcnt(0)
	v_mfma_f32_16x16x32_bf16 v[166:169], v[58:61], v[128:131], 0
	v_mfma_f32_16x16x32_bf16 v[166:169], v[62:65], v[132:135], v[166:169]
	v_mfma_f32_16x16x32_bf16 v[166:169], v[66:69], v[136:139], v[166:169]
	v_mfma_f32_16x16x32_bf16 v[166:169], v[70:73], v[140:143], v[166:169]
	s_waitcnt lgkmcnt(14)
	ds_read_b128 v[150:153], v21 offset:25600
	s_waitcnt lgkmcnt(14)
	ds_read_b128 v[154:157], v21 offset:25664
	s_waitcnt lgkmcnt(14)
	ds_read_b128 v[158:161], v21 offset:25728
	s_waitcnt lgkmcnt(14)
	ds_read_b128 v[162:165], v21 offset:25792
	v_mfma_f32_16x16x32_bf16 v[170:173], v[74:77], v[128:131], 0
	v_mfma_f32_16x16x32_bf16 v[170:173], v[78:81], v[132:135], v[170:173]
	v_mfma_f32_16x16x32_bf16 v[170:173], v[82:85], v[136:139], v[170:173]
	v_mfma_f32_16x16x32_bf16 v[170:173], v[86:89], v[140:143], v[170:173]
	s_waitcnt lgkmcnt(12)
	v_mfma_f32_16x16x32_bf16 v[174:177], v[90:93], v[128:131], 0
	v_mfma_f32_16x16x32_bf16 v[174:177], v[94:97], v[132:135], v[174:177]
	v_mfma_f32_16x16x32_bf16 v[174:177], v[98:101], v[136:139], v[174:177]
	v_mfma_f32_16x16x32_bf16 v[174:177], v[146:149], v[140:143], v[174:177]
	s_waitcnt lgkmcnt(0)
	v_mfma_f32_16x16x32_bf16 v[178:181], v[150:153], v[128:131], 0
	v_mfma_f32_16x16x32_bf16 v[178:181], v[154:157], v[132:135], v[178:181]
	v_mfma_f32_16x16x32_bf16 v[178:181], v[158:161], v[136:139], v[178:181]
	v_mfma_f32_16x16x32_bf16 v[178:181], v[162:165], v[140:143], v[178:181]
	v_mad_u32_u24 v10, v20, s18, v17
	v_readlane_b32 s18, v255, 19
	ds_write_b32 v110, v166 offset:512
	ds_write_b32 v110, v167 offset:1540
	ds_write_b32 v110, v168 offset:2568
	ds_write_b32 v110, v169 offset:3596
	ds_write_b32 v110, v170 offset:16960
	ds_write_b32 v110, v171 offset:17988
	ds_write_b32 v110, v172 offset:19016
	ds_write_b32 v110, v173 offset:20044
	ds_write_b32 v110, v174 offset:33408
	ds_write_b32 v110, v175 offset:34436
	ds_write_b32 v110, v176 offset:35464
	ds_write_b32 v110, v177 offset:36492
	s_nop 1
	ds_write_b32 v110, v178 offset:49856
	ds_write_b32 v110, v179 offset:50884
	ds_write_b32 v110, v180 offset:51912
	s_waitcnt lgkmcnt(14)
	ds_write_b32 v110, v181 offset:52940
	v_add_u32_e32 v0, 0x8400, v10
	s_waitcnt lgkmcnt(0)
	s_barrier
	ds_read2_b32 v[0:1], v0 offset1:1
	s_waitcnt lgkmcnt(0)
	v_not_b32_e32 v2, v0
	v_or_b32_e32 v3, 0x80000000, v0
	v_cmp_gt_i32_e32 vcc, 0, v0
	s_nop 1
	v_cndmask_b32_e32 v0, v3, v2, vcc
	v_and_b32_e32 v0, 0xffffff80, v0
	v_or_b32_e32 v6, s18, v0
	v_add_u32_e32 v0, 0x8440, v10
	ds_read2_b32 v[2:3], v0 offset1:1
	v_readlane_b32 s18, v255, 6
	s_waitcnt lgkmcnt(0)
	v_not_b32_e32 v0, v2
	v_or_b32_e32 v4, 0x80000000, v2
	v_cmp_gt_i32_e32 vcc, 0, v2
	v_or_b32_e32 v2, 0x80000000, v1
	s_nop 0
	v_cndmask_b32_e32 v0, v4, v0, vcc
	v_and_b32_e32 v0, 0xffffff80, v0
	v_or_b32_e32 v4, s18, v0
	v_not_b32_e32 v0, v1
	v_cmp_gt_i32_e32 vcc, 0, v1
	v_readlane_b32 s18, v255, 8
	v_or_b32_e32 v1, 0x80000000, v3
	v_cndmask_b32_e32 v0, v2, v0, vcc
	v_and_b32_e32 v0, 0xffffff80, v0
	v_or_b32_e32 v7, s18, v0
	v_not_b32_e32 v0, v3
	v_cmp_gt_i32_e32 vcc, 0, v3
	v_readlane_b32 s18, v255, 10
	s_nop 0
	v_cndmask_b32_e32 v0, v1, v0, vcc
	v_and_b32_e32 v0, 0xffffff80, v0
	v_or_b32_e32 v5, s18, v0
	v_add_u32_e32 v0, 0x8408, v10
	ds_read2_b32 v[0:1], v0 offset1:1
	v_readlane_b32 s18, v255, 14
	v_max_u32_e32 v49, v4, v5
	v_min_u32_e32 v4, v4, v5
	s_waitcnt lgkmcnt(0)
	v_not_b32_e32 v2, v0
	v_or_b32_e32 v3, 0x80000000, v0
	v_cmp_gt_i32_e32 vcc, 0, v0
	s_nop 1
	v_cndmask_b32_e32 v0, v3, v2, vcc
	v_and_b32_e32 v0, 0xffffff80, v0
	v_or_b32_e32 v11, s18, v0
	v_add_u32_e32 v0, 0x8448, v10
	ds_read2_b32 v[2:3], v0 offset1:1
	v_readlane_b32 s18, v255, 16
	s_waitcnt lgkmcnt(0)
	v_not_b32_e32 v0, v2
	v_or_b32_e32 v8, 0x80000000, v2
	v_cmp_gt_i32_e32 vcc, 0, v2
	v_or_b32_e32 v2, 0x80000000, v1
	s_nop 0
	v_cndmask_b32_e32 v0, v8, v0, vcc
	v_and_b32_e32 v0, 0xffffff80, v0
	v_or_b32_e32 v8, s18, v0
	v_not_b32_e32 v0, v1
	v_cmp_gt_i32_e32 vcc, 0, v1
	v_readlane_b32 s18, v255, 23
	v_or_b32_e32 v1, 0x80000000, v3
	v_cndmask_b32_e32 v0, v2, v0, vcc
	v_and_b32_e32 v0, 0xffffff80, v0
	v_or_b32_e32 v23, s18, v0
	v_not_b32_e32 v0, v3
	v_cmp_gt_i32_e32 vcc, 0, v3
	v_readlane_b32 s18, v255, 24
	s_nop 0
	v_cndmask_b32_e32 v0, v1, v0, vcc
	v_and_b32_e32 v0, 0xffffff80, v0
	v_or_b32_e32 v9, s18, v0
	v_add_u32_e32 v0, 0x8410, v10
	ds_read2_b32 v[0:1], v0 offset1:1
	v_readlane_b32 s18, v255, 25
	v_max_u32_e32 v5, v8, v9
	v_min_u32_e32 v8, v8, v9
	s_waitcnt lgkmcnt(0)
	v_not_b32_e32 v2, v0
	v_or_b32_e32 v3, 0x80000000, v0
	v_cmp_gt_i32_e32 vcc, 0, v0
	s_nop 1
	v_cndmask_b32_e32 v0, v3, v2, vcc
	v_and_b32_e32 v0, 0xffffff80, v0
	v_or_b32_e32 v24, s18, v0
	v_add_u32_e32 v0, 0x8450, v10
	ds_read2_b32 v[2:3], v0 offset1:1
	v_readlane_b32 s18, v255, 26
	s_waitcnt lgkmcnt(0)
	v_not_b32_e32 v0, v2
	v_or_b32_e32 v21, 0x80000000, v2
	v_cmp_gt_i32_e32 vcc, 0, v2
	v_or_b32_e32 v2, 0x80000000, v1
	s_nop 0
	v_cndmask_b32_e32 v0, v21, v0, vcc
	v_and_b32_e32 v0, 0xffffff80, v0
	v_or_b32_e32 v21, s18, v0
	v_not_b32_e32 v0, v1
	v_cmp_gt_i32_e32 vcc, 0, v1
	v_readlane_b32 s18, v255, 27
	v_or_b32_e32 v1, 0x80000000, v3
	v_cndmask_b32_e32 v0, v2, v0, vcc
	v_and_b32_e32 v0, 0xffffff80, v0
	v_or_b32_e32 v27, s18, v0
	v_not_b32_e32 v0, v3
	v_cmp_gt_i32_e32 vcc, 0, v3
	v_readlane_b32 s18, v255, 28
	s_nop 0
	v_cndmask_b32_e32 v0, v1, v0, vcc
	v_and_b32_e32 v0, 0xffffff80, v0
	v_or_b32_e32 v22, s18, v0
	v_add_u32_e32 v0, 0x8418, v10
	ds_read2_b32 v[0:1], v0 offset1:1
	v_readlane_b32 s18, v255, 29
	v_max_u32_e32 v9, v21, v22
	v_min_u32_e32 v21, v21, v22
	s_waitcnt lgkmcnt(0)
	v_not_b32_e32 v2, v0
	v_or_b32_e32 v3, 0x80000000, v0
	v_cmp_gt_i32_e32 vcc, 0, v0
	s_nop 1
	v_cndmask_b32_e32 v0, v3, v2, vcc
	v_and_b32_e32 v0, 0xffffff80, v0
	v_or_b32_e32 v28, s18, v0
	v_add_u32_e32 v0, 0x8458, v10
	ds_read2_b32 v[2:3], v0 offset1:1
	v_readlane_b32 s18, v255, 30
	s_waitcnt lgkmcnt(0)
	v_not_b32_e32 v0, v2
	v_or_b32_e32 v25, 0x80000000, v2
	v_cmp_gt_i32_e32 vcc, 0, v2
	v_or_b32_e32 v2, 0x80000000, v1
	s_nop 0
	v_cndmask_b32_e32 v0, v25, v0, vcc
	v_and_b32_e32 v0, 0xffffff80, v0
	v_or_b32_e32 v25, s18, v0
	v_not_b32_e32 v0, v1
	v_cmp_gt_i32_e32 vcc, 0, v1
	v_readlane_b32 s18, v255, 31
	v_or_b32_e32 v1, 0x80000000, v3
	v_cndmask_b32_e32 v0, v2, v0, vcc
	v_and_b32_e32 v0, 0xffffff80, v0
	v_or_b32_e32 v31, s18, v0
	v_not_b32_e32 v0, v3
	v_cmp_gt_i32_e32 vcc, 0, v3
	v_readlane_b32 s18, v255, 32
	s_nop 0
	v_cndmask_b32_e32 v0, v1, v0, vcc
	v_and_b32_e32 v0, 0xffffff80, v0
	v_or_b32_e32 v26, s56, v0
	v_add_u32_e32 v0, 0x8420, v10
	ds_read2_b32 v[0:1], v0 offset1:1
	v_max_u32_e32 v22, v25, v26
	v_min_u32_e32 v25, v25, v26
	s_waitcnt lgkmcnt(0)
	v_not_b32_e32 v2, v0
	v_or_b32_e32 v3, 0x80000000, v0
	v_cmp_gt_i32_e32 vcc, 0, v0
	s_nop 1
	v_cndmask_b32_e32 v0, v3, v2, vcc
	v_and_b32_e32 v0, 0xffffff80, v0
	v_or_b32_e32 v32, s18, v0
	v_add_u32_e32 v0, 0x8460, v10
	ds_read2_b32 v[2:3], v0 offset1:1
	s_movk_i32 s18, 0x800
	s_waitcnt lgkmcnt(0)
	v_not_b32_e32 v0, v2
	v_or_b32_e32 v29, 0x80000000, v2
	v_cmp_gt_i32_e32 vcc, 0, v2
	v_or_b32_e32 v2, 0x80000000, v1
	s_nop 0
	v_cndmask_b32_e32 v0, v29, v0, vcc
	v_and_b32_e32 v0, 0xffffff80, v0
	v_or_b32_e32 v29, s85, v0
	v_not_b32_e32 v0, v1
	v_cmp_gt_i32_e32 vcc, 0, v1
	v_or_b32_e32 v1, 0x80000000, v3
	s_nop 0
	v_cndmask_b32_e32 v0, v2, v0, vcc
	v_and_b32_e32 v0, 0xffffff80, v0
	v_or_b32_e32 v33, s49, v0
	v_not_b32_e32 v0, v3
	v_cmp_gt_i32_e32 vcc, 0, v3
	s_nop 1
	v_cndmask_b32_e32 v0, v1, v0, vcc
	v_and_b32_e32 v0, 0xffffff80, v0
	v_or_b32_e32 v30, s60, v0
	v_add_u32_e32 v0, 0x8428, v10
	ds_read2_b32 v[0:1], v0 offset1:1
	v_max_u32_e32 v26, v29, v30
	v_min_u32_e32 v29, v29, v30
	s_waitcnt lgkmcnt(0)
	v_not_b32_e32 v2, v0
	v_or_b32_e32 v3, 0x80000000, v0
	v_cmp_gt_i32_e32 vcc, 0, v0
	s_nop 1
	v_cndmask_b32_e32 v0, v3, v2, vcc
	v_add_u32_e32 v2, 0x8468, v10
	ds_read2_b32 v[2:3], v2 offset1:1
	v_and_b32_e32 v0, 0xffffff80, v0
	v_or_b32_e32 v0, s62, v0
	s_waitcnt lgkmcnt(0)
	v_not_b32_e32 v34, v2
	v_or_b32_e32 v35, 0x80000000, v2
	v_cmp_gt_i32_e32 vcc, 0, v2
	s_nop 1
	v_cndmask_b32_e32 v2, v35, v34, vcc
	v_and_b32_e32 v2, 0xffffff80, v2
	v_or_b32_e32 v36, s63, v2
	v_not_b32_e32 v2, v1
	v_or_b32_e32 v34, 0x80000000, v1
	v_cmp_gt_i32_e32 vcc, 0, v1
	s_nop 1
	v_cndmask_b32_e32 v1, v34, v2, vcc
	v_not_b32_e32 v2, v3
	v_or_b32_e32 v34, 0x80000000, v3
	v_cmp_gt_i32_e32 vcc, 0, v3
	v_and_b32_e32 v1, 0xffffff80, v1
	v_or_b32_e32 v1, s64, v1
	v_cndmask_b32_e32 v2, v34, v2, vcc
	v_and_b32_e32 v2, 0xffffff80, v2
	v_or_b32_e32 v37, s65, v2
	v_add_u32_e32 v2, 0x8430, v10
	ds_read2_b32 v[2:3], v2 offset1:1
	v_max_u32_e32 v30, v36, v37
	v_min_u32_e32 v36, v36, v37
	s_waitcnt lgkmcnt(0)
	v_not_b32_e32 v34, v2
	v_or_b32_e32 v35, 0x80000000, v2
	v_cmp_gt_i32_e32 vcc, 0, v2
	s_nop 1
	v_cndmask_b32_e32 v2, v35, v34, vcc
	v_and_b32_e32 v2, 0xffffff80, v2
	v_or_b32_e32 v38, s66, v2
	v_add_u32_e32 v2, 0x8470, v10
	ds_read2_b32 v[34:35], v2 offset1:1
	s_waitcnt lgkmcnt(0)
	v_not_b32_e32 v2, v34
	v_or_b32_e32 v39, 0x80000000, v34
	v_cmp_gt_i32_e32 vcc, 0, v34
	v_or_b32_e32 v34, 0x80000000, v3
	s_nop 0
	v_cndmask_b32_e32 v2, v39, v2, vcc
	v_and_b32_e32 v2, 0xffffff80, v2
	v_or_b32_e32 v39, s67, v2
	v_not_b32_e32 v2, v3
	v_cmp_gt_i32_e32 vcc, 0, v3
	v_or_b32_e32 v3, 0x80000000, v35
	s_nop 0
	v_cndmask_b32_e32 v2, v34, v2, vcc
	v_and_b32_e32 v2, 0xffffff80, v2
	v_or_b32_e32 v40, s42, v2
	v_not_b32_e32 v2, v35
	v_cmp_gt_i32_e32 vcc, 0, v35
	s_nop 1
	v_cndmask_b32_e32 v2, v3, v2, vcc
	v_and_b32_e32 v2, 0xffffff80, v2
	v_or_b32_e32 v41, s96, v2
	v_add_u32_e32 v2, 0x8438, v10
	ds_read2_b32 v[2:3], v2 offset1:1
	v_add_u32_e32 v10, 0x8478, v10
	v_max_u32_e32 v37, v39, v41
	v_min_u32_e32 v39, v39, v41
	s_waitcnt lgkmcnt(0)
	v_not_b32_e32 v34, v2
	v_or_b32_e32 v35, 0x80000000, v2
	v_cmp_gt_i32_e32 vcc, 0, v2
	s_nop 1
	v_cndmask_b32_e32 v2, v35, v34, vcc
	ds_read2_b32 v[34:35], v10 offset1:1
	v_and_b32_e32 v2, 0xffffff80, v2
	v_or_b32_e32 v2, s97, v2
	s_waitcnt lgkmcnt(0)
	v_not_b32_e32 v10, v34
	v_or_b32_e32 v42, 0x80000000, v34
	v_cmp_gt_i32_e32 vcc, 0, v34
	v_not_b32_e32 v34, v3
	s_nop 0
	v_cndmask_b32_e32 v10, v42, v10, vcc
	v_or_b32_e32 v42, 0x80000000, v3
	v_cmp_gt_i32_e32 vcc, 0, v3
	v_and_b32_e32 v10, 0xffffff80, v10
	v_or_b32_e32 v10, s45, v10
	v_cndmask_b32_e32 v3, v42, v34, vcc
	v_not_b32_e32 v34, v35
	v_or_b32_e32 v42, 0x80000000, v35
	v_cmp_gt_i32_e32 vcc, 0, v35
	v_and_b32_e32 v3, 0xffffff80, v3
	v_or_b32_e32 v3, s53, v3
	v_cndmask_b32_e32 v34, v42, v34, vcc
	v_and_b32_e32 v34, 0xffffff80, v34
	v_or_b32_e32 v34, s24, v34
	v_max_u32_e32 v35, v6, v7
	v_min_u32_e32 v6, v6, v7
	v_max_u32_e32 v7, v11, v23
	v_min_u32_e32 v11, v11, v23
	v_max_u32_e32 v23, v24, v27
	v_min_u32_e32 v24, v24, v27
	v_max_u32_e32 v27, v28, v31
	v_min_u32_e32 v28, v28, v31
	v_max_u32_e32 v31, v32, v33
	v_min_u32_e32 v32, v32, v33
	v_max_u32_e32 v33, v0, v1
	v_min_u32_e32 v0, v0, v1
	v_max_u32_e32 v1, v38, v40
	v_min_u32_e32 v38, v38, v40
	v_max_u32_e32 v40, v2, v3
	v_min_u32_e32 v2, v2, v3
	v_max_u32_e32 v41, v10, v34
	v_min_u32_e32 v10, v10, v34
	v_max_u32_e32 v3, v35, v11
	v_min_u32_e32 v11, v35, v11
	v_max_u32_e32 v35, v6, v7
	v_min_u32_e32 v6, v6, v7
	v_max_u32_e32 v7, v23, v28
	v_min_u32_e32 v23, v23, v28
	v_max_u32_e32 v28, v24, v27
	v_min_u32_e32 v24, v24, v27
	v_max_u32_e32 v27, v31, v0
	v_min_u32_e32 v0, v31, v0
	v_max_u32_e32 v31, v32, v33
	v_min_u32_e32 v32, v32, v33
	v_max_u32_e32 v33, v1, v2
	v_min_u32_e32 v1, v1, v2
	v_max_u32_e32 v2, v38, v40
	v_min_u32_e32 v38, v38, v40
	v_max_u32_e32 v34, v49, v8
	v_min_u32_e32 v8, v49, v8
	v_max_u32_e32 v49, v4, v5
	v_min_u32_e32 v4, v4, v5
	v_max_u32_e32 v5, v9, v25
	v_min_u32_e32 v9, v9, v25
	v_max_u32_e32 v25, v21, v22
	v_min_u32_e32 v21, v21, v22
	v_max_u32_e32 v22, v26, v36
	v_min_u32_e32 v26, v26, v36
	v_max_u32_e32 v36, v29, v30
	v_min_u32_e32 v29, v29, v30
	v_max_u32_e32 v30, v37, v10
	v_min_u32_e32 v10, v37, v10
	v_max_u32_e32 v37, v39, v41
	v_min_u32_e32 v39, v39, v41
	v_max_u32_e32 v40, v3, v35
	v_min_u32_e32 v3, v3, v35
	v_max_u32_e32 v35, v11, v6
	v_min_u32_e32 v6, v11, v6
	v_max_u32_e32 v11, v23, v24
	v_min_u32_e32 v23, v23, v24
	v_max_u32_e32 v24, v7, v28
	v_min_u32_e32 v7, v7, v28
	v_max_u32_e32 v28, v27, v31
	v_min_u32_e32 v27, v27, v31
	v_max_u32_e32 v31, v0, v32
	v_min_u32_e32 v0, v0, v32
	v_max_u32_e32 v32, v1, v38
	v_min_u32_e32 v1, v1, v38
	v_max_u32_e32 v38, v33, v2
	v_min_u32_e32 v2, v33, v2
	v_max_u32_e32 v41, v34, v49
	v_min_u32_e32 v34, v34, v49
	v_max_u32_e32 v49, v8, v4
	v_min_u32_e32 v4, v8, v4
	v_max_u32_e32 v8, v9, v21
	v_min_u32_e32 v9, v9, v21
	v_max_u32_e32 v21, v5, v25
	v_min_u32_e32 v5, v5, v25
	v_max_u32_e32 v25, v22, v36
	v_min_u32_e32 v22, v22, v36
	v_max_u32_e32 v36, v26, v29
	v_min_u32_e32 v26, v26, v29
	v_max_u32_e32 v29, v10, v39
	v_min_u32_e32 v10, v10, v39
	v_max_u32_e32 v39, v30, v37
	v_min_u32_e32 v30, v30, v37
	v_max_u32_e32 v33, v40, v23
	v_min_u32_e32 v23, v40, v23
	v_max_u32_e32 v40, v3, v11
	v_min_u32_e32 v3, v3, v11
	v_max_u32_e32 v11, v35, v7
	v_min_u32_e32 v7, v35, v7
	v_max_u32_e32 v35, v6, v24
	v_min_u32_e32 v6, v6, v24
	v_max_u32_e32 v24, v28, v1
	v_min_u32_e32 v1, v28, v1
	v_max_u32_e32 v28, v27, v32
	v_min_u32_e32 v27, v27, v32
	v_max_u32_e32 v32, v31, v2
	v_min_u32_e32 v2, v31, v2
	v_max_u32_e32 v31, v0, v38
	v_min_u32_e32 v0, v0, v38
	v_max_u32_e32 v37, v41, v9
	v_min_u32_e32 v9, v41, v9
	v_max_u32_e32 v41, v34, v8
	v_min_u32_e32 v8, v34, v8
	v_max_u32_e32 v34, v49, v5
	v_min_u32_e32 v5, v49, v5
	v_max_u32_e32 v49, v4, v21
	v_min_u32_e32 v4, v4, v21
	v_max_u32_e32 v21, v25, v10
	v_min_u32_e32 v10, v25, v10
	v_max_u32_e32 v25, v22, v29
	v_min_u32_e32 v22, v22, v29
	v_max_u32_e32 v29, v36, v30
	v_min_u32_e32 v30, v36, v30
	v_max_u32_e32 v36, v26, v39
	v_min_u32_e32 v26, v26, v39
	v_max_u32_e32 v38, v33, v11
	v_min_u32_e32 v11, v33, v11
	v_max_u32_e32 v33, v40, v35
	v_min_u32_e32 v35, v40, v35
	v_max_u32_e32 v40, v23, v7
	v_min_u32_e32 v7, v23, v7
	v_max_u32_e32 v23, v3, v6
	v_min_u32_e32 v3, v3, v6
	v_max_u32_e32 v6, v1, v2
	v_min_u32_e32 v1, v1, v2
	v_max_u32_e32 v2, v27, v0
	v_min_u32_e32 v0, v27, v0
	v_max_u32_e32 v27, v24, v32
	v_min_u32_e32 v24, v24, v32
	v_max_u32_e32 v32, v28, v31
	v_min_u32_e32 v28, v28, v31
	v_max_u32_e32 v39, v37, v34
	v_min_u32_e32 v34, v37, v34
	v_max_u32_e32 v37, v41, v49
	v_min_u32_e32 v41, v41, v49
	v_max_u32_e32 v49, v9, v5
	v_min_u32_e32 v5, v9, v5
	v_max_u32_e32 v9, v8, v4
	v_min_u32_e32 v4, v8, v4
	v_max_u32_e32 v8, v10, v30
	v_min_u32_e32 v10, v10, v30
	v_max_u32_e32 v30, v22, v26
	v_min_u32_e32 v22, v22, v26
	v_max_u32_e32 v26, v21, v29
	v_min_u32_e32 v21, v21, v29
	v_max_u32_e32 v29, v25, v36
	v_min_u32_e32 v25, v25, v36
	v_max_u32_e32 v31, v38, v33
	v_min_u32_e32 v33, v38, v33
	v_max_u32_e32 v38, v11, v35
	v_min_u32_e32 v11, v11, v35
	v_max_u32_e32 v35, v40, v23
	v_min_u32_e32 v23, v40, v23
	v_max_u32_e32 v40, v7, v3
	v_min_u32_e32 v3, v7, v3
	v_max_u32_e32 v7, v1, v0
	v_min_u32_e32 v0, v1, v0
	v_max_u32_e32 v1, v6, v2
	v_min_u32_e32 v2, v6, v2
	v_max_u32_e32 v6, v24, v28
	v_min_u32_e32 v24, v24, v28
	v_max_u32_e32 v28, v27, v32
	v_min_u32_e32 v27, v27, v32
	v_max_u32_e32 v36, v39, v37
	v_min_u32_e32 v37, v39, v37
	v_max_u32_e32 v39, v34, v41
	v_min_u32_e32 v34, v34, v41
	v_max_u32_e32 v41, v49, v9
	v_min_u32_e32 v9, v49, v9
	v_max_u32_e32 v49, v5, v4
	v_min_u32_e32 v4, v5, v4
	v_max_u32_e32 v5, v10, v22
	v_min_u32_e32 v10, v10, v22
	v_max_u32_e32 v22, v8, v30
	v_min_u32_e32 v8, v8, v30
	v_max_u32_e32 v30, v21, v25
	v_min_u32_e32 v21, v21, v25
	v_max_u32_e32 v25, v26, v29
	v_min_u32_e32 v26, v26, v29
	v_max_u32_e32 v32, v31, v0
	v_min_u32_e32 v0, v31, v0
	v_max_u32_e32 v31, v33, v7
	v_min_u32_e32 v7, v33, v7
	v_max_u32_e32 v33, v38, v2
	v_min_u32_e32 v2, v38, v2
	v_max_u32_e32 v38, v11, v1
	v_min_u32_e32 v1, v11, v1
	v_max_u32_e32 v11, v35, v24
	v_min_u32_e32 v24, v35, v24
	v_max_u32_e32 v35, v23, v6
	v_min_u32_e32 v6, v23, v6
	v_max_u32_e32 v23, v40, v27
	v_min_u32_e32 v27, v40, v27
	v_max_u32_e32 v40, v3, v28
	v_min_u32_e32 v3, v3, v28
	v_max_u32_e32 v29, v36, v10
	v_min_u32_e32 v10, v36, v10
	v_max_u32_e32 v36, v37, v5
	v_min_u32_e32 v5, v37, v5
	v_max_u32_e32 v37, v39, v8
	v_min_u32_e32 v8, v39, v8
	v_max_u32_e32 v39, v34, v22
	v_min_u32_e32 v22, v34, v22
	v_max_u32_e32 v34, v41, v21
	v_min_u32_e32 v21, v41, v21
	v_max_u32_e32 v41, v9, v30
	v_min_u32_e32 v9, v9, v30
	v_max_u32_e32 v30, v49, v26
	v_min_u32_e32 v26, v49, v26
	v_max_u32_e32 v49, v4, v25
	v_min_u32_e32 v4, v4, v25
	v_max_u32_e32 v28, v32, v11
	v_min_u32_e32 v11, v32, v11
	v_max_u32_e32 v32, v31, v35
	v_min_u32_e32 v31, v31, v35
	v_max_u32_e32 v35, v33, v23
	v_min_u32_e32 v23, v33, v23
	v_max_u32_e32 v33, v38, v40
	v_min_u32_e32 v38, v38, v40
	v_max_u32_e32 v40, v0, v24
	v_min_u32_e32 v0, v0, v24
	v_max_u32_e32 v24, v7, v6
	v_min_u32_e32 v6, v7, v6
	v_max_u32_e32 v7, v2, v27
	v_min_u32_e32 v2, v2, v27
	v_max_u32_e32 v27, v1, v3
	v_min_u32_e32 v1, v1, v3
	v_max_u32_e32 v25, v29, v34
	v_min_u32_e32 v29, v29, v34
	v_max_u32_e32 v34, v36, v41
	v_min_u32_e32 v36, v36, v41
	v_max_u32_e32 v41, v37, v30
	v_min_u32_e32 v30, v37, v30
	v_max_u32_e32 v37, v39, v49
	v_min_u32_e32 v39, v39, v49
	v_max_u32_e32 v49, v10, v21
	v_min_u32_e32 v10, v10, v21
	v_max_u32_e32 v21, v5, v9
	v_min_u32_e32 v5, v5, v9
	v_max_u32_e32 v9, v8, v26
	v_min_u32_e32 v8, v8, v26
	v_max_u32_e32 v26, v22, v4
	v_min_u32_e32 v4, v22, v4
	v_max_u32_e32 v3, v28, v35
	v_min_u32_e32 v28, v28, v35
	v_max_u32_e32 v35, v32, v33
	v_min_u32_e32 v32, v32, v33
	v_max_u32_e32 v33, v11, v23
	v_min_u32_e32 v11, v11, v23
	v_max_u32_e32 v23, v31, v38
	v_min_u32_e32 v31, v31, v38
	v_max_u32_e32 v38, v40, v7
	v_min_u32_e32 v7, v40, v7
	v_max_u32_e32 v40, v24, v27
	v_min_u32_e32 v24, v24, v27
	v_max_u32_e32 v27, v0, v2
	v_min_u32_e32 v0, v0, v2
	v_max_u32_e32 v2, v6, v1
	v_min_u32_e32 v1, v6, v1
	v_max_u32_e32 v22, v25, v41
	v_min_u32_e32 v25, v25, v41
	v_max_u32_e32 v41, v34, v37
	v_min_u32_e32 v34, v34, v37
	v_max_u32_e32 v37, v29, v30
	v_min_u32_e32 v29, v29, v30
	v_max_u32_e32 v30, v36, v39
	v_min_u32_e32 v36, v36, v39
	v_max_u32_e32 v39, v49, v9
	v_min_u32_e32 v9, v49, v9
	v_max_u32_e32 v49, v21, v26
	v_min_u32_e32 v21, v21, v26
	v_max_u32_e32 v26, v10, v8
	v_min_u32_e32 v8, v10, v8
	v_max_u32_e32 v10, v5, v4
	v_min_u32_e32 v4, v5, v4
	v_min_u32_e32 v6, v3, v35
	v_min_u32_e32 v42, v28, v32
	v_min_u32_e32 v43, v33, v23
	v_min_u32_e32 v44, v11, v31
	v_min_u32_e32 v45, v38, v40
	v_min_u32_e32 v46, v7, v24
	v_min_u32_e32 v47, v27, v2
	v_min_u32_e32 v48, v0, v1
	v_min_u32_e32 v5, v22, v41
	v_min_u32_e32 v50, v25, v34
	v_min_u32_e32 v51, v37, v30
	v_min_u32_e32 v52, v29, v36
	v_min_u32_e32 v53, v39, v49
	v_min_u32_e32 v54, v9, v21
	v_min_u32_e32 v55, v26, v10
	v_min_u32_e32 v56, v8, v4
	v_max3_u32 v3, v3, v35, v56
	v_max3_u32 v4, v6, v8, v4
	v_max3_u32 v6, v28, v32, v55
	v_max3_u32 v8, v42, v26, v10
	v_max3_u32 v10, v33, v23, v54
	v_max3_u32 v9, v43, v9, v21
	v_max3_u32 v11, v11, v31, v53
	v_max3_u32 v21, v44, v39, v49
	v_max3_u32 v23, v38, v40, v52
	v_max3_u32 v26, v45, v29, v36
	v_max3_u32 v7, v7, v24, v51
	v_max3_u32 v24, v46, v37, v30
	v_max3_u32 v2, v27, v2, v50
	v_max3_u32 v25, v47, v25, v34
	v_max3_u32 v0, v0, v1, v5
	v_max3_u32 v1, v48, v22, v41
	v_max_u32_e32 v5, v3, v23
	v_min_u32_e32 v3, v3, v23
	v_max_u32_e32 v22, v4, v26
	v_min_u32_e32 v4, v4, v26
	v_max_u32_e32 v23, v6, v7
	v_min_u32_e32 v6, v6, v7
	v_max_u32_e32 v7, v8, v24
	v_min_u32_e32 v8, v8, v24
	v_max_u32_e32 v24, v10, v2
	v_min_u32_e32 v2, v10, v2
	v_max_u32_e32 v10, v9, v25
	v_min_u32_e32 v9, v9, v25
	v_max_u32_e32 v25, v11, v0
	v_min_u32_e32 v0, v11, v0
	v_max_u32_e32 v11, v21, v1
	v_min_u32_e32 v1, v21, v1
	v_max_u32_e32 v21, v5, v24
	v_min_u32_e32 v5, v5, v24
	v_max_u32_e32 v24, v22, v10
	v_min_u32_e32 v10, v22, v10
	v_max_u32_e32 v22, v23, v25
	v_min_u32_e32 v23, v23, v25
	v_max_u32_e32 v25, v7, v11
	v_min_u32_e32 v7, v7, v11
	v_max_u32_e32 v11, v3, v2
	v_min_u32_e32 v2, v3, v2
	v_max_u32_e32 v3, v4, v9
	v_min_u32_e32 v4, v4, v9
	v_max_u32_e32 v9, v6, v0
	v_min_u32_e32 v0, v6, v0
	v_max_u32_e32 v6, v8, v1
	v_min_u32_e32 v1, v8, v1
	v_max_u32_e32 v8, v21, v22
	v_min_u32_e32 v21, v21, v22
	v_max_u32_e32 v22, v24, v25
	v_min_u32_e32 v24, v24, v25
	v_max_u32_e32 v25, v5, v23
	v_min_u32_e32 v5, v5, v23
	v_max_u32_e32 v23, v10, v7
	v_min_u32_e32 v7, v10, v7
	v_max_u32_e32 v10, v11, v9
	v_min_u32_e32 v9, v11, v9
	v_max_u32_e32 v11, v3, v6
	v_min_u32_e32 v3, v3, v6
	v_max_u32_e32 v6, v2, v0
	v_min_u32_e32 v0, v2, v0
	v_max_u32_e32 v2, v4, v1
	v_min_u32_e32 v1, v4, v1
	v_mov_b32_e32 v43, s84
	v_max_u32_e32 v41, v0, v1
	v_min_u32_e32 v42, v0, v1
	v_bitop3_b32 v1, v20, s18, v43 bitop3:0x36
	v_max_u32_e32 v28, v8, v22
	v_min_u32_e32 v29, v8, v22
	v_lshl_add_u32 v0, v20, 2, v18
	v_lshl_add_u32 v1, v1, 2, v12
	v_max_u32_e32 v30, v21, v24
	v_min_u32_e32 v21, v21, v24
	v_max_u32_e32 v31, v25, v23
	v_min_u32_e32 v32, v25, v23
	v_max_u32_e32 v33, v5, v7
	v_min_u32_e32 v34, v5, v7
	v_max_u32_e32 v35, v10, v11
	v_min_u32_e32 v36, v10, v11
	v_max_u32_e32 v37, v9, v3
	v_min_u32_e32 v38, v9, v3
	v_max_u32_e32 v39, v6, v2
	v_min_u32_e32 v40, v6, v2
	ds_write2st64_b32 v0, v28, v29 offset1:1
	ds_write2st64_b32 v0, v30, v21 offset0:2 offset1:3
	ds_write2st64_b32 v0, v31, v32 offset0:4 offset1:5
	ds_write2st64_b32 v0, v33, v34 offset0:6 offset1:7
	ds_write2st64_b32 v0, v35, v36 offset0:8 offset1:9
	ds_write2st64_b32 v0, v37, v38 offset0:10 offset1:11
	ds_write2st64_b32 v0, v39, v40 offset0:12 offset1:13
	ds_write2st64_b32 v0, v41, v42 offset0:14 offset1:15
	s_waitcnt lgkmcnt(0)
	s_barrier
	ds_read2st64_b32 v[2:3], v1 offset1:1
	ds_read2st64_b32 v[4:5], v1 offset0:2 offset1:3
	ds_read2st64_b32 v[6:7], v1 offset0:4 offset1:5
	ds_read2st64_b32 v[8:9], v1 offset0:6 offset1:7
	ds_read2st64_b32 v[10:11], v1 offset0:8 offset1:9
	ds_read2st64_b32 v[22:23], v1 offset0:10 offset1:11
	ds_read2st64_b32 v[24:25], v1 offset0:12 offset1:13
	ds_read2st64_b32 v[26:27], v1 offset0:14 offset1:15
	s_waitcnt lgkmcnt(4)
	v_max_u32_e32 v9, v35, v9
	s_waitcnt lgkmcnt(3)
	v_max_u32_e32 v11, v33, v11
	s_waitcnt lgkmcnt(2)
	v_max_u32_e32 v23, v31, v23
	s_waitcnt lgkmcnt(1)
	v_max_u32_e32 v25, v30, v25
	s_waitcnt lgkmcnt(0)
	v_max_u32_e32 v27, v28, v27
	v_max_u32_e32 v26, v29, v26
	v_max_u32_e32 v21, v21, v24
	v_max_u32_e32 v22, v32, v22
	v_max_u32_e32 v10, v34, v10
	v_max_u32_e32 v8, v36, v8
	v_max_u32_e32 v7, v37, v7
	v_max_u32_e32 v6, v38, v6
	v_max_u32_e32 v5, v39, v5
	v_max_u32_e32 v4, v40, v4
	v_max_u32_e32 v3, v41, v3
	v_max_u32_e32 v2, v42, v2
	v_max_u32_e32 v24, v27, v9
	v_min_u32_e32 v9, v27, v9
	v_max_u32_e32 v27, v26, v8
	v_min_u32_e32 v8, v26, v8
	v_max_u32_e32 v26, v25, v7
	v_min_u32_e32 v7, v25, v7
	v_max_u32_e32 v25, v21, v6
	v_min_u32_e32 v6, v21, v6
	v_max_u32_e32 v21, v23, v5
	v_min_u32_e32 v5, v23, v5
	v_max_u32_e32 v23, v22, v4
	v_min_u32_e32 v4, v22, v4
	v_max_u32_e32 v22, v11, v3
	v_min_u32_e32 v3, v11, v3
	v_max_u32_e32 v11, v10, v2
	v_min_u32_e32 v2, v10, v2
	v_max_u32_e32 v10, v24, v21
	v_min_u32_e32 v21, v24, v21
	v_max_u32_e32 v24, v27, v23
	v_min_u32_e32 v23, v27, v23
	v_max_u32_e32 v27, v26, v22
	v_min_u32_e32 v22, v26, v22
	v_max_u32_e32 v26, v25, v11
	v_min_u32_e32 v11, v25, v11
	v_max_u32_e32 v25, v9, v5
	v_min_u32_e32 v5, v9, v5
	v_max_u32_e32 v9, v8, v4
	v_min_u32_e32 v4, v8, v4
	v_max_u32_e32 v8, v7, v3
	v_min_u32_e32 v3, v7, v3
	v_max_u32_e32 v7, v6, v2
	v_min_u32_e32 v2, v6, v2
	v_max_u32_e32 v6, v10, v27
	v_min_u32_e32 v10, v10, v27
	v_max_u32_e32 v27, v24, v26
	v_min_u32_e32 v24, v24, v26
	v_max_u32_e32 v28, v21, v22
	v_min_u32_e32 v22, v21, v22
	v_max_u32_e32 v21, v23, v11
	v_min_u32_e32 v29, v23, v11
	v_max_u32_e32 v30, v25, v8
	v_min_u32_e32 v8, v25, v8
	v_max_u32_e32 v25, v9, v7
	v_min_u32_e32 v7, v9, v7
	v_min_u32_e32 v32, v5, v3
	v_max_u32_e32 v33, v4, v2
	v_min_u32_e32 v2, v4, v2
	s_movk_i32 s18, 0x1000
	v_max_u32_e32 v31, v5, v3
	v_max_u32_e32 v26, v6, v27
	v_min_u32_e32 v5, v6, v27
	v_max_u32_e32 v11, v10, v24
	v_min_u32_e32 v3, v10, v24
	v_max_u32_e32 v23, v28, v21
	v_min_u32_e32 v6, v28, v21
	v_max_u32_e32 v21, v22, v29
	v_min_u32_e32 v4, v22, v29
	v_max_u32_e32 v22, v8, v7
	v_min_u32_e32 v7, v8, v7
	v_max_u32_e32 v24, v32, v2
	v_min_u32_e32 v8, v32, v2
	v_bitop3_b32 v2, v20, s18, v43 bitop3:0x36
	v_max_u32_e32 v27, v30, v25
	v_min_u32_e32 v9, v30, v25
	v_max_u32_e32 v25, v31, v33
	v_min_u32_e32 v10, v31, v33
	v_lshl_add_u32 v2, v2, 2, v12
	s_and_b64 vcc, exec, s[34:35]
	ds_write2st64_b32 v0, v26, v5 offset0:132 offset1:133
	ds_write2st64_b32 v0, v11, v3 offset0:134 offset1:135
	ds_write2st64_b32 v0, v23, v6 offset0:136 offset1:137
	ds_write2st64_b32 v0, v21, v4 offset0:138 offset1:139
	ds_write2st64_b32 v0, v27, v9 offset0:140 offset1:141
	ds_write2st64_b32 v0, v22, v7 offset0:142 offset1:143
	ds_write2st64_b32 v0, v25, v10 offset0:144 offset1:145
	ds_write2st64_b32 v0, v24, v8 offset0:146 offset1:147
	s_waitcnt lgkmcnt(0)
	s_barrier
	s_cbranch_vccz .LBB0_979
	ds_read2st64_b32 v[28:29], v2 offset0:146 offset1:147
	ds_read2st64_b32 v[30:31], v2 offset0:138 offset1:139
	ds_read2st64_b32 v[32:33], v2 offset0:142 offset1:143
	ds_read2st64_b32 v[34:35], v2 offset0:144 offset1:145
	ds_read2st64_b32 v[36:37], v2 offset0:134 offset1:135
	ds_read2st64_b32 v[38:39], v2 offset0:136 offset1:137
	s_waitcnt lgkmcnt(5)
	v_max_u32_e32 v29, v26, v29
	s_waitcnt lgkmcnt(4)
	v_max_u32_e32 v31, v27, v31
	ds_read2st64_b32 v[26:27], v2 offset0:140 offset1:141
	ds_read2st64_b32 v[40:41], v2 offset0:132 offset1:133
	s_waitcnt lgkmcnt(5)
	v_max_u32_e32 v23, v23, v33
	s_waitcnt lgkmcnt(3)
	v_max_u32_e32 v25, v25, v37
	v_max_u32_e32 v11, v11, v35
	s_waitcnt lgkmcnt(2)
	v_max_u32_e32 v22, v22, v39
	s_waitcnt lgkmcnt(1)
	v_max_u32_e32 v21, v21, v27
	s_waitcnt lgkmcnt(0)
	v_max_u32_e32 v24, v24, v41
	v_max_u32_e32 v5, v5, v28
	v_max_u32_e32 v9, v9, v30
	v_max_u32_e32 v6, v6, v32
	v_max_u32_e32 v10, v10, v36
	v_max_u32_e32 v3, v3, v34
	v_max_u32_e32 v7, v7, v38
	v_max_u32_e32 v4, v4, v26
	v_max_u32_e32 v8, v8, v40
	v_min_u32_e32 v42, v29, v31
	v_min_u32_e32 v33, v23, v25
	v_min_u32_e32 v35, v11, v22
	v_min_u32_e32 v27, v21, v24
	v_min_u32_e32 v28, v5, v9
	v_min_u32_e32 v30, v6, v10
	v_min_u32_e32 v34, v3, v7
	v_min_u32_e32 v26, v4, v8
	v_min_u32_e32 v37, v42, v33
	v_min_u32_e32 v39, v35, v27
	v_min_u32_e32 v32, v28, v30
	v_min_u32_e32 v36, v34, v26
	v_max_u32_e32 v33, v42, v33
	v_max_u32_e32 v27, v35, v27
	v_max_u32_e32 v28, v28, v30
	v_max_u32_e32 v26, v34, v26
	v_min_u32_e32 v35, v33, v27
	v_min_u32_e32 v30, v28, v26
	v_max_u32_e32 v27, v33, v27
	v_max_u32_e32 v26, v28, v26
	v_min_u32_e32 v28, v27, v26
	v_max_u32_e32 v26, v27, v26
	v_max_u32_e32 v27, v29, v31
	v_max_u32_e32 v23, v23, v25
	v_max_u32_e32 v11, v11, v22
	v_max_u32_e32 v21, v21, v24
	v_max_u32_e32 v5, v5, v9
	v_max_u32_e32 v6, v6, v10
	v_max_u32_e32 v3, v3, v7
	v_max_u32_e32 v4, v4, v8
	v_min_u32_e32 v25, v27, v23
	v_min_u32_e32 v22, v11, v21
	v_min_u32_e32 v9, v5, v6
	v_min_u32_e32 v7, v3, v4
	v_min_u32_e32 v24, v25, v22
	v_min_u32_e32 v8, v9, v7
	v_max_u32_e32 v22, v25, v22
	v_max_u32_e32 v7, v9, v7
	v_min_u32_e32 v9, v22, v7
	v_max_u32_e32 v7, v22, v7
	v_max_u32_e32 v22, v27, v23
	v_max_u32_e32 v11, v11, v21
	v_max_u32_e32 v5, v5, v6
	v_max_u32_e32 v3, v3, v4
	v_min_u32_e32 v21, v22, v11
	v_min_u32_e32 v4, v5, v3
	v_max_u32_e32 v11, v22, v11
	v_max_u32_e32 v3, v5, v3
	v_min_u32_e32 v41, v37, v39
	v_min_u32_e32 v38, v32, v36
	v_max_u32_e32 v37, v37, v39
	v_max_u32_e32 v32, v32, v36
	v_min_u32_e32 v5, v11, v3
	v_max_u32_e32 v3, v11, v3
	v_lshl_add_u32 v11, v20, 2, v19
	v_min_u32_e32 v40, v41, v38
	v_max_u32_e32 v38, v41, v38
	v_min_u32_e32 v36, v37, v32
	v_max_u32_e32 v32, v37, v32
	v_min_u32_e32 v34, v35, v30
	v_max_u32_e32 v30, v35, v30
	v_min_u32_e32 v10, v24, v8
	v_max_u32_e32 v8, v24, v8
	v_min_u32_e32 v6, v21, v4
	v_max_u32_e32 v4, v21, v4
	ds_write2st64_b32 v11, v3, v5 offset1:1
	ds_write2st64_b32 v11, v4, v6 offset0:2 offset1:3
	ds_write2st64_b32 v11, v7, v9 offset0:4 offset1:5
	ds_write2st64_b32 v11, v8, v10 offset0:6 offset1:7
	ds_write2st64_b32 v11, v26, v28 offset0:8 offset1:9
	ds_write2st64_b32 v11, v30, v34 offset0:10 offset1:11
	ds_write2st64_b32 v11, v32, v36 offset0:12 offset1:13
	ds_write2st64_b32 v11, v38, v40 offset0:14 offset1:15

.LBB0_1036:
	s_or_b64 exec, exec, s[18:19]
	s_lshl_b32 s18, s26, 16
	v_readlane_b32 s19, v255, 18
	v_and_b32_e32 v10, 15, v2
	s_or_b32 s18, s18, s19
	v_readlane_b32 s19, v255, 4
	v_or_b32_e32 v0, s62, v10
	s_add_u32 s18, s19, s18
	v_readlane_b32 s19, v255, 12
	v_ashrrev_i32_e32 v1, 31, v0
	s_addc_u32 s19, s19, 0
	v_lshlrev_b64 v[0:1], 8, v[0:1]
	v_lshl_add_u64 v[0:1], s[18:19], 0, v[0:1]
	v_and_b32_e32 v104, 48, v2
	v_and_b32_e32 v20, 63, v2
	v_lshl_add_u64 v[0:1], v[0:1], 0, v[104:105]
	v_lshrrev_b32_e32 v2, 2, v2
	s_waitcnt lgkmcnt(0)
	s_barrier
	v_and_b32_e32 v11, 12, v2
	global_load_dwordx4 v[112:115], v[0:1], off
	global_load_dwordx4 v[116:119], v[0:1], off offset:64
	global_load_dwordx4 v[120:123], v[0:1], off offset:128
	global_load_dwordx4 v[124:127], v[0:1], off offset:192
	s_mov_b32 s19, 0x8000
	v_add_co_u32_e32 v24, vcc, s19, v0
	v_lshl_add_u32 v23, v10, 2, v16
	v_mul_u32_u24_e32 v10, 0x210, v10
	v_addc_co_u32_e32 v25, vcc, 0, v1, vcc
	v_add3_u32 v21, v12, v104, v10
	global_load_dwordx4 v[128:131], v[24:25], off
	global_load_dwordx4 v[132:135], v[24:25], off offset:64
	global_load_dwordx4 v[136:139], v[24:25], off offset:128
	global_load_dwordx4 v[140:143], v[24:25], off offset:192
	ds_read_b128 v[58:61], v21
	ds_read_b128 v[62:65], v21 offset:64
	ds_read_b128 v[66:69], v21 offset:128
	ds_read_b128 v[70:73], v21 offset:192
	ds_read_b128 v[74:77], v21 offset:8448
	ds_read_b128 v[78:81], v21 offset:8512
	ds_read_b128 v[82:85], v21 offset:8576
	ds_read_b128 v[86:89], v21 offset:8640
	ds_read_b128 v[90:93], v21 offset:16896
	ds_read_b128 v[94:97], v21 offset:16960
	ds_read_b128 v[98:101], v21 offset:17024
	ds_read_b128 v[146:149], v21 offset:17088
	s_movk_i32 s18, 0x404
	v_mad_u32_u24 v22, v11, s18, v23
	v_add_u32_e32 v110, 0x8400, v22
	s_waitcnt vmcnt(4) lgkmcnt(8)
	v_mfma_f32_16x16x32_bf16 v[166:169], v[58:61], v[112:115], 0
	v_mfma_f32_16x16x32_bf16 v[166:169], v[62:65], v[116:119], v[166:169]
	v_mfma_f32_16x16x32_bf16 v[166:169], v[66:69], v[120:123], v[166:169]
	v_mfma_f32_16x16x32_bf16 v[166:169], v[70:73], v[124:127], v[166:169]
	ds_read_b128 v[150:153], v21 offset:25344
	ds_read_b128 v[154:157], v21 offset:25408
	ds_read_b128 v[158:161], v21 offset:25472
	ds_read_b128 v[162:165], v21 offset:25536
	s_waitcnt lgkmcnt(8)
	v_mfma_f32_16x16x32_bf16 v[170:173], v[74:77], v[112:115], 0
	v_mfma_f32_16x16x32_bf16 v[170:173], v[78:81], v[116:119], v[170:173]
	v_mfma_f32_16x16x32_bf16 v[170:173], v[82:85], v[120:123], v[170:173]
	v_mfma_f32_16x16x32_bf16 v[170:173], v[86:89], v[124:127], v[170:173]
	s_waitcnt lgkmcnt(4)
	v_mfma_f32_16x16x32_bf16 v[174:177], v[90:93], v[112:115], 0
	v_mfma_f32_16x16x32_bf16 v[174:177], v[94:97], v[116:119], v[174:177]
	v_mfma_f32_16x16x32_bf16 v[174:177], v[98:101], v[120:123], v[174:177]
	v_mfma_f32_16x16x32_bf16 v[174:177], v[146:149], v[124:127], v[174:177]
	s_waitcnt lgkmcnt(0)
	v_mfma_f32_16x16x32_bf16 v[178:181], v[150:153], v[112:115], 0
	v_mfma_f32_16x16x32_bf16 v[178:181], v[154:157], v[116:119], v[178:181]
	v_mfma_f32_16x16x32_bf16 v[178:181], v[158:161], v[120:123], v[178:181]
	v_mfma_f32_16x16x32_bf16 v[178:181], v[162:165], v[124:127], v[178:181]
	ds_read_b128 v[58:61], v21 offset:256
	ds_read_b128 v[62:65], v21 offset:320
	ds_read_b128 v[66:69], v21 offset:384
	ds_read_b128 v[70:73], v21 offset:448
	ds_read_b128 v[74:77], v21 offset:8704
	ds_read_b128 v[78:81], v21 offset:8768
	ds_read_b128 v[82:85], v21 offset:8832
	ds_read_b128 v[86:89], v21 offset:8896
	ds_write_b32 v110, v166 offset:0
	ds_write_b32 v110, v167 offset:1028
	ds_write_b32 v110, v168 offset:2056
	ds_write_b32 v110, v169 offset:3084
	ds_write_b32 v110, v170 offset:16448
	ds_write_b32 v110, v171 offset:17476
	ds_write_b32 v110, v172 offset:18504
	s_waitcnt lgkmcnt(14)
	ds_write_b32 v110, v173 offset:19532
	s_waitcnt lgkmcnt(14)
	ds_read_b128 v[90:93], v21 offset:17152
	s_waitcnt lgkmcnt(14)
	ds_read_b128 v[94:97], v21 offset:17216
	s_waitcnt lgkmcnt(14)
	ds_read_b128 v[98:101], v21 offset:17280
	s_waitcnt lgkmcnt(14)
	ds_read_b128 v[146:149], v21 offset:17344
	s_waitcnt lgkmcnt(14)
	ds_write_b32 v110, v174 offset:32896
	s_waitcnt lgkmcnt(14)
	ds_write_b32 v110, v175 offset:33924
	s_waitcnt lgkmcnt(14)
	ds_write_b32 v110, v176 offset:34952
	s_waitcnt lgkmcnt(14)
	ds_write_b32 v110, v177 offset:35980
	s_nop 3
	s_waitcnt lgkmcnt(14)
	ds_write_b32 v110, v178 offset:49344
	s_waitcnt lgkmcnt(14)
	ds_write_b32 v110, v179 offset:50372
	s_waitcnt lgkmcnt(14)
	ds_write_b32 v110, v180 offset:51400
	s_waitcnt lgkmcnt(14)
	ds_write_b32 v110, v181 offset:52428
	s_waitcnt vmcnt(0)
	v_mfma_f32_16x16x32_bf16 v[166:169], v[58:61], v[128:131], 0
	v_mfma_f32_16x16x32_bf16 v[166:169], v[62:65], v[132:135], v[166:169]
	v_mfma_f32_16x16x32_bf16 v[166:169], v[66:69], v[136:139], v[166:169]
	v_mfma_f32_16x16x32_bf16 v[166:169], v[70:73], v[140:143], v[166:169]
	s_waitcnt lgkmcnt(14)
	ds_read_b128 v[150:153], v21 offset:25600
	s_waitcnt lgkmcnt(14)
	ds_read_b128 v[154:157], v21 offset:25664
	s_waitcnt lgkmcnt(14)
	ds_read_b128 v[158:161], v21 offset:25728
	s_waitcnt lgkmcnt(14)
	ds_read_b128 v[162:165], v21 offset:25792
	v_mfma_f32_16x16x32_bf16 v[170:173], v[74:77], v[128:131], 0
	v_mfma_f32_16x16x32_bf16 v[170:173], v[78:81], v[132:135], v[170:173]
	v_mfma_f32_16x16x32_bf16 v[170:173], v[82:85], v[136:139], v[170:173]
	v_mfma_f32_16x16x32_bf16 v[170:173], v[86:89], v[140:143], v[170:173]
	s_waitcnt lgkmcnt(12)
	v_mfma_f32_16x16x32_bf16 v[174:177], v[90:93], v[128:131], 0
	v_mfma_f32_16x16x32_bf16 v[174:177], v[94:97], v[132:135], v[174:177]
	v_mfma_f32_16x16x32_bf16 v[174:177], v[98:101], v[136:139], v[174:177]
	v_mfma_f32_16x16x32_bf16 v[174:177], v[146:149], v[140:143], v[174:177]
	s_waitcnt lgkmcnt(0)
	v_mfma_f32_16x16x32_bf16 v[178:181], v[150:153], v[128:131], 0
	v_mfma_f32_16x16x32_bf16 v[178:181], v[154:157], v[132:135], v[178:181]
	v_mfma_f32_16x16x32_bf16 v[178:181], v[158:161], v[136:139], v[178:181]
	v_mfma_f32_16x16x32_bf16 v[178:181], v[162:165], v[140:143], v[178:181]
	v_mad_u32_u24 v10, v20, s18, v17
	v_readlane_b32 s18, v255, 19
	ds_write_b32 v110, v166 offset:512
	ds_write_b32 v110, v167 offset:1540
	ds_write_b32 v110, v168 offset:2568
	ds_write_b32 v110, v169 offset:3596
	ds_write_b32 v110, v170 offset:16960
	ds_write_b32 v110, v171 offset:17988
	ds_write_b32 v110, v172 offset:19016
	ds_write_b32 v110, v173 offset:20044
	ds_write_b32 v110, v174 offset:33408
	ds_write_b32 v110, v175 offset:34436
	ds_write_b32 v110, v176 offset:35464
	ds_write_b32 v110, v177 offset:36492
	s_nop 1
	ds_write_b32 v110, v178 offset:49856
	ds_write_b32 v110, v179 offset:50884
	ds_write_b32 v110, v180 offset:51912
	s_waitcnt lgkmcnt(14)
	ds_write_b32 v110, v181 offset:52940
	v_add_u32_e32 v0, 0x8400, v10
	s_waitcnt lgkmcnt(0)
	s_barrier
	ds_read2_b32 v[0:1], v0 offset1:1
	s_waitcnt lgkmcnt(0)
	v_not_b32_e32 v2, v0
	v_or_b32_e32 v3, 0x80000000, v0
	v_cmp_gt_i32_e32 vcc, 0, v0
	s_nop 1
	v_cndmask_b32_e32 v0, v3, v2, vcc
	v_and_b32_e32 v0, 0xffffff80, v0
	v_or_b32_e32 v6, s18, v0
	v_add_u32_e32 v0, 0x8440, v10
	ds_read2_b32 v[2:3], v0 offset1:1
	v_readlane_b32 s18, v255, 6
	s_waitcnt lgkmcnt(0)
	v_not_b32_e32 v0, v2
	v_or_b32_e32 v4, 0x80000000, v2
	v_cmp_gt_i32_e32 vcc, 0, v2
	v_or_b32_e32 v2, 0x80000000, v1
	s_nop 0
	v_cndmask_b32_e32 v0, v4, v0, vcc
	v_and_b32_e32 v0, 0xffffff80, v0
	v_or_b32_e32 v4, s18, v0
	v_not_b32_e32 v0, v1
	v_cmp_gt_i32_e32 vcc, 0, v1
	v_readlane_b32 s18, v255, 8
	v_or_b32_e32 v1, 0x80000000, v3
	v_cndmask_b32_e32 v0, v2, v0, vcc
	v_and_b32_e32 v0, 0xffffff80, v0
	v_or_b32_e32 v7, s18, v0
	v_not_b32_e32 v0, v3
	v_cmp_gt_i32_e32 vcc, 0, v3
	v_readlane_b32 s18, v255, 10
	s_nop 0
	v_cndmask_b32_e32 v0, v1, v0, vcc
	v_and_b32_e32 v0, 0xffffff80, v0
	v_or_b32_e32 v5, s18, v0
	v_add_u32_e32 v0, 0x8408, v10
	ds_read2_b32 v[0:1], v0 offset1:1
	v_readlane_b32 s18, v255, 14
	v_max_u32_e32 v49, v4, v5
	v_min_u32_e32 v4, v4, v5
	s_waitcnt lgkmcnt(0)
	v_not_b32_e32 v2, v0
	v_or_b32_e32 v3, 0x80000000, v0
	v_cmp_gt_i32_e32 vcc, 0, v0
	s_nop 1
	v_cndmask_b32_e32 v0, v3, v2, vcc
	v_and_b32_e32 v0, 0xffffff80, v0
	v_or_b32_e32 v11, s18, v0
	v_add_u32_e32 v0, 0x8448, v10
	ds_read2_b32 v[2:3], v0 offset1:1
	v_readlane_b32 s18, v255, 16
	s_waitcnt lgkmcnt(0)
	v_not_b32_e32 v0, v2
	v_or_b32_e32 v8, 0x80000000, v2
	v_cmp_gt_i32_e32 vcc, 0, v2
	v_or_b32_e32 v2, 0x80000000, v1
	s_nop 0
	v_cndmask_b32_e32 v0, v8, v0, vcc
	v_and_b32_e32 v0, 0xffffff80, v0
	v_or_b32_e32 v8, s18, v0
	v_not_b32_e32 v0, v1
	v_cmp_gt_i32_e32 vcc, 0, v1
	v_readlane_b32 s18, v255, 23
	v_or_b32_e32 v1, 0x80000000, v3
	v_cndmask_b32_e32 v0, v2, v0, vcc
	v_and_b32_e32 v0, 0xffffff80, v0
	v_or_b32_e32 v23, s18, v0
	v_not_b32_e32 v0, v3
	v_cmp_gt_i32_e32 vcc, 0, v3
	v_readlane_b32 s18, v255, 24
	s_nop 0
	v_cndmask_b32_e32 v0, v1, v0, vcc
	v_and_b32_e32 v0, 0xffffff80, v0
	v_or_b32_e32 v9, s18, v0
	v_add_u32_e32 v0, 0x8410, v10
	ds_read2_b32 v[0:1], v0 offset1:1
	v_readlane_b32 s18, v255, 25
	v_max_u32_e32 v5, v8, v9
	v_min_u32_e32 v8, v8, v9
	s_waitcnt lgkmcnt(0)
	v_not_b32_e32 v2, v0
	v_or_b32_e32 v3, 0x80000000, v0
	v_cmp_gt_i32_e32 vcc, 0, v0
	s_nop 1
	v_cndmask_b32_e32 v0, v3, v2, vcc
	v_and_b32_e32 v0, 0xffffff80, v0
	v_or_b32_e32 v24, s18, v0
	v_add_u32_e32 v0, 0x8450, v10
	ds_read2_b32 v[2:3], v0 offset1:1
	v_readlane_b32 s18, v255, 26
	s_waitcnt lgkmcnt(0)
	v_not_b32_e32 v0, v2
	v_or_b32_e32 v21, 0x80000000, v2
	v_cmp_gt_i32_e32 vcc, 0, v2
	v_or_b32_e32 v2, 0x80000000, v1
	s_nop 0
	v_cndmask_b32_e32 v0, v21, v0, vcc
	v_and_b32_e32 v0, 0xffffff80, v0
	v_or_b32_e32 v21, s18, v0
	v_not_b32_e32 v0, v1
	v_cmp_gt_i32_e32 vcc, 0, v1
	v_readlane_b32 s18, v255, 27
	v_or_b32_e32 v1, 0x80000000, v3
	v_cndmask_b32_e32 v0, v2, v0, vcc
	v_and_b32_e32 v0, 0xffffff80, v0
	v_or_b32_e32 v27, s18, v0
	v_not_b32_e32 v0, v3
	v_cmp_gt_i32_e32 vcc, 0, v3
	v_readlane_b32 s18, v255, 28
	s_nop 0
	v_cndmask_b32_e32 v0, v1, v0, vcc
	v_and_b32_e32 v0, 0xffffff80, v0
	v_or_b32_e32 v22, s18, v0
	v_add_u32_e32 v0, 0x8418, v10
	ds_read2_b32 v[0:1], v0 offset1:1
	v_readlane_b32 s18, v255, 29
	v_max_u32_e32 v9, v21, v22
	v_min_u32_e32 v21, v21, v22
	s_waitcnt lgkmcnt(0)
	v_not_b32_e32 v2, v0
	v_or_b32_e32 v3, 0x80000000, v0
	v_cmp_gt_i32_e32 vcc, 0, v0
	s_nop 1
	v_cndmask_b32_e32 v0, v3, v2, vcc
	v_and_b32_e32 v0, 0xffffff80, v0
	v_or_b32_e32 v28, s18, v0
	v_add_u32_e32 v0, 0x8458, v10
	ds_read2_b32 v[2:3], v0 offset1:1
	v_readlane_b32 s18, v255, 30
	s_waitcnt lgkmcnt(0)
	v_not_b32_e32 v0, v2
	v_or_b32_e32 v25, 0x80000000, v2
	v_cmp_gt_i32_e32 vcc, 0, v2
	v_or_b32_e32 v2, 0x80000000, v1
	s_nop 0
	v_cndmask_b32_e32 v0, v25, v0, vcc
	v_and_b32_e32 v0, 0xffffff80, v0
	v_or_b32_e32 v25, s18, v0
	v_not_b32_e32 v0, v1
	v_cmp_gt_i32_e32 vcc, 0, v1
	v_readlane_b32 s18, v255, 31
	v_or_b32_e32 v1, 0x80000000, v3
	v_cndmask_b32_e32 v0, v2, v0, vcc
	v_and_b32_e32 v0, 0xffffff80, v0
	v_or_b32_e32 v31, s18, v0
	v_not_b32_e32 v0, v3
	v_cmp_gt_i32_e32 vcc, 0, v3
	v_readlane_b32 s18, v255, 32
	s_nop 0
	v_cndmask_b32_e32 v0, v1, v0, vcc
	v_and_b32_e32 v0, 0xffffff80, v0
	v_or_b32_e32 v26, s18, v0
	v_add_u32_e32 v0, 0x8420, v10
	ds_read2_b32 v[0:1], v0 offset1:1
	v_readlane_b32 s18, v255, 22
	v_max_u32_e32 v22, v25, v26
	v_min_u32_e32 v25, v25, v26
	s_waitcnt lgkmcnt(0)
	v_not_b32_e32 v2, v0
	v_or_b32_e32 v3, 0x80000000, v0
	v_cmp_gt_i32_e32 vcc, 0, v0
	s_nop 1
	v_cndmask_b32_e32 v0, v3, v2, vcc
	v_and_b32_e32 v0, 0xffffff80, v0
	v_or_b32_e32 v32, s18, v0
	v_add_u32_e32 v0, 0x8460, v10
	ds_read2_b32 v[2:3], v0 offset1:1
	v_readlane_b32 s18, v255, 20
	s_waitcnt lgkmcnt(0)
	v_not_b32_e32 v0, v2
	v_or_b32_e32 v29, 0x80000000, v2
	v_cmp_gt_i32_e32 vcc, 0, v2
	v_or_b32_e32 v2, 0x80000000, v1
	s_nop 0
	v_cndmask_b32_e32 v0, v29, v0, vcc
	v_and_b32_e32 v0, 0xffffff80, v0
	v_or_b32_e32 v29, s18, v0
	v_not_b32_e32 v0, v1
	v_cmp_gt_i32_e32 vcc, 0, v1
	v_readlane_b32 s18, v255, 35
	v_or_b32_e32 v1, 0x80000000, v3
	v_cndmask_b32_e32 v0, v2, v0, vcc
	v_and_b32_e32 v0, 0xffffff80, v0
	v_or_b32_e32 v33, s18, v0
	v_not_b32_e32 v0, v3
	v_cmp_gt_i32_e32 vcc, 0, v3
	v_readlane_b32 s18, v255, 37
	s_nop 0
	v_cndmask_b32_e32 v0, v1, v0, vcc
	v_and_b32_e32 v0, 0xffffff80, v0
	v_or_b32_e32 v30, s18, v0
	v_add_u32_e32 v0, 0x8428, v10
	ds_read2_b32 v[0:1], v0 offset1:1
	v_readlane_b32 s18, v255, 38
	v_max_u32_e32 v26, v29, v30
	v_min_u32_e32 v29, v29, v30
	s_waitcnt lgkmcnt(0)
	v_not_b32_e32 v2, v0
	v_or_b32_e32 v3, 0x80000000, v0
	v_cmp_gt_i32_e32 vcc, 0, v0
	s_nop 1
	v_cndmask_b32_e32 v0, v3, v2, vcc
	v_add_u32_e32 v2, 0x8468, v10
	ds_read2_b32 v[2:3], v2 offset1:1
	v_and_b32_e32 v0, 0xffffff80, v0
	v_or_b32_e32 v0, s18, v0
	s_movk_i32 s18, 0x800
	s_waitcnt lgkmcnt(0)
	v_not_b32_e32 v34, v2
	v_or_b32_e32 v35, 0x80000000, v2
	v_cmp_gt_i32_e32 vcc, 0, v2
	s_nop 1
	v_cndmask_b32_e32 v2, v35, v34, vcc
	v_and_b32_e32 v2, 0xffffff80, v2
	v_or_b32_e32 v36, s49, v2
	v_not_b32_e32 v2, v1
	v_or_b32_e32 v34, 0x80000000, v1
	v_cmp_gt_i32_e32 vcc, 0, v1
	s_nop 1
	v_cndmask_b32_e32 v1, v34, v2, vcc
	v_not_b32_e32 v2, v3
	v_or_b32_e32 v34, 0x80000000, v3
	v_cmp_gt_i32_e32 vcc, 0, v3
	v_and_b32_e32 v1, 0xffffff80, v1
	v_or_b32_e32 v1, s56, v1
	v_cndmask_b32_e32 v2, v34, v2, vcc
	v_and_b32_e32 v2, 0xffffff80, v2
	v_or_b32_e32 v37, s57, v2
	v_add_u32_e32 v2, 0x8430, v10
	ds_read2_b32 v[2:3], v2 offset1:1
	v_max_u32_e32 v30, v36, v37
	v_min_u32_e32 v36, v36, v37
	s_waitcnt lgkmcnt(0)
	v_not_b32_e32 v34, v2
	v_or_b32_e32 v35, 0x80000000, v2
	v_cmp_gt_i32_e32 vcc, 0, v2
	s_nop 1
	v_cndmask_b32_e32 v2, v35, v34, vcc
	v_and_b32_e32 v2, 0xffffff80, v2
	v_or_b32_e32 v38, s60, v2
	v_add_u32_e32 v2, 0x8470, v10
	ds_read2_b32 v[34:35], v2 offset1:1
	s_waitcnt lgkmcnt(0)
	v_not_b32_e32 v2, v34
	v_or_b32_e32 v39, 0x80000000, v34
	v_cmp_gt_i32_e32 vcc, 0, v34
	v_or_b32_e32 v34, 0x80000000, v3
	s_nop 0
	v_cndmask_b32_e32 v2, v39, v2, vcc
	v_and_b32_e32 v2, 0xffffff80, v2
	v_or_b32_e32 v39, s61, v2
	v_not_b32_e32 v2, v3
	v_cmp_gt_i32_e32 vcc, 0, v3
	v_or_b32_e32 v3, 0x80000000, v35
	s_nop 0
	v_cndmask_b32_e32 v2, v34, v2, vcc
	v_and_b32_e32 v2, 0xffffff80, v2
	v_or_b32_e32 v40, s42, v2
	v_not_b32_e32 v2, v35
	v_cmp_gt_i32_e32 vcc, 0, v35
	s_nop 1
	v_cndmask_b32_e32 v2, v3, v2, vcc
	v_and_b32_e32 v2, 0xffffff80, v2
	v_or_b32_e32 v41, s63, v2
	v_add_u32_e32 v2, 0x8438, v10
	ds_read2_b32 v[2:3], v2 offset1:1
	v_add_u32_e32 v10, 0x8478, v10
	v_max_u32_e32 v37, v39, v41
	v_min_u32_e32 v39, v39, v41
	s_waitcnt lgkmcnt(0)
	v_not_b32_e32 v34, v2
	v_or_b32_e32 v35, 0x80000000, v2
	v_cmp_gt_i32_e32 vcc, 0, v2
	s_nop 1
	v_cndmask_b32_e32 v2, v35, v34, vcc
	ds_read2_b32 v[34:35], v10 offset1:1
	v_and_b32_e32 v2, 0xffffff80, v2
	v_or_b32_e32 v2, s64, v2
	s_waitcnt lgkmcnt(0)
	v_not_b32_e32 v10, v34
	v_or_b32_e32 v42, 0x80000000, v34
	v_cmp_gt_i32_e32 vcc, 0, v34
	v_not_b32_e32 v34, v3
	s_nop 0
	v_cndmask_b32_e32 v10, v42, v10, vcc
	v_or_b32_e32 v42, 0x80000000, v3
	v_cmp_gt_i32_e32 vcc, 0, v3
	v_and_b32_e32 v10, 0xffffff80, v10
	v_or_b32_e32 v10, s65, v10
	v_cndmask_b32_e32 v3, v42, v34, vcc
	v_not_b32_e32 v34, v35
	v_or_b32_e32 v42, 0x80000000, v35
	v_cmp_gt_i32_e32 vcc, 0, v35
	v_and_b32_e32 v3, 0xffffff80, v3
	v_or_b32_e32 v3, s66, v3
	v_cndmask_b32_e32 v34, v42, v34, vcc
	v_and_b32_e32 v34, 0xffffff80, v34
	v_or_b32_e32 v34, s67, v34
	v_max_u32_e32 v35, v6, v7
	v_min_u32_e32 v6, v6, v7
	v_max_u32_e32 v7, v11, v23
	v_min_u32_e32 v11, v11, v23
	v_max_u32_e32 v23, v24, v27
	v_min_u32_e32 v24, v24, v27
	v_max_u32_e32 v27, v28, v31
	v_min_u32_e32 v28, v28, v31
	v_max_u32_e32 v31, v32, v33
	v_min_u32_e32 v32, v32, v33
	v_max_u32_e32 v33, v0, v1
	v_min_u32_e32 v0, v0, v1
	v_max_u32_e32 v1, v38, v40
	v_min_u32_e32 v38, v38, v40
	v_max_u32_e32 v40, v2, v3
	v_min_u32_e32 v2, v2, v3
	v_max_u32_e32 v41, v10, v34
	v_min_u32_e32 v10, v10, v34
	v_max_u32_e32 v3, v35, v11
	v_min_u32_e32 v11, v35, v11
	v_max_u32_e32 v35, v6, v7
	v_min_u32_e32 v6, v6, v7
	v_max_u32_e32 v7, v23, v28
	v_min_u32_e32 v23, v23, v28
	v_max_u32_e32 v28, v24, v27
	v_min_u32_e32 v24, v24, v27
	v_max_u32_e32 v27, v31, v0
	v_min_u32_e32 v0, v31, v0
	v_max_u32_e32 v31, v32, v33
	v_min_u32_e32 v32, v32, v33
	v_max_u32_e32 v33, v1, v2
	v_min_u32_e32 v1, v1, v2
	v_max_u32_e32 v2, v38, v40
	v_min_u32_e32 v38, v38, v40
	v_max_u32_e32 v34, v49, v8
	v_min_u32_e32 v8, v49, v8
	v_max_u32_e32 v49, v4, v5
	v_min_u32_e32 v4, v4, v5
	v_max_u32_e32 v5, v9, v25
	v_min_u32_e32 v9, v9, v25
	v_max_u32_e32 v25, v21, v22
	v_min_u32_e32 v21, v21, v22
	v_max_u32_e32 v22, v26, v36
	v_min_u32_e32 v26, v26, v36
	v_max_u32_e32 v36, v29, v30
	v_min_u32_e32 v29, v29, v30
	v_max_u32_e32 v30, v37, v10
	v_min_u32_e32 v10, v37, v10
	v_max_u32_e32 v37, v39, v41
	v_min_u32_e32 v39, v39, v41
	v_max_u32_e32 v40, v3, v35
	v_min_u32_e32 v3, v3, v35
	v_max_u32_e32 v35, v11, v6
	v_min_u32_e32 v6, v11, v6
	v_max_u32_e32 v11, v23, v24
	v_min_u32_e32 v23, v23, v24
	v_max_u32_e32 v24, v7, v28
	v_min_u32_e32 v7, v7, v28
	v_max_u32_e32 v28, v27, v31
	v_min_u32_e32 v27, v27, v31
	v_max_u32_e32 v31, v0, v32
	v_min_u32_e32 v0, v0, v32
	v_max_u32_e32 v32, v1, v38
	v_min_u32_e32 v1, v1, v38
	v_max_u32_e32 v38, v33, v2
	v_min_u32_e32 v2, v33, v2
	v_max_u32_e32 v41, v34, v49
	v_min_u32_e32 v34, v34, v49
	v_max_u32_e32 v49, v8, v4
	v_min_u32_e32 v4, v8, v4
	v_max_u32_e32 v8, v9, v21
	v_min_u32_e32 v9, v9, v21
	v_max_u32_e32 v21, v5, v25
	v_min_u32_e32 v5, v5, v25
	v_max_u32_e32 v25, v22, v36
	v_min_u32_e32 v22, v22, v36
	v_max_u32_e32 v36, v26, v29
	v_min_u32_e32 v26, v26, v29
	v_max_u32_e32 v29, v10, v39
	v_min_u32_e32 v10, v10, v39
	v_max_u32_e32 v39, v30, v37
	v_min_u32_e32 v30, v30, v37
	v_max_u32_e32 v33, v40, v23
	v_min_u32_e32 v23, v40, v23
	v_max_u32_e32 v40, v3, v11
	v_min_u32_e32 v3, v3, v11
	v_max_u32_e32 v11, v35, v7
	v_min_u32_e32 v7, v35, v7
	v_max_u32_e32 v35, v6, v24
	v_min_u32_e32 v6, v6, v24
	v_max_u32_e32 v24, v28, v1
	v_min_u32_e32 v1, v28, v1
	v_max_u32_e32 v28, v27, v32
	v_min_u32_e32 v27, v27, v32
	v_max_u32_e32 v32, v31, v2
	v_min_u32_e32 v2, v31, v2
	v_max_u32_e32 v31, v0, v38
	v_min_u32_e32 v0, v0, v38
	v_max_u32_e32 v37, v41, v9
	v_min_u32_e32 v9, v41, v9
	v_max_u32_e32 v41, v34, v8
	v_min_u32_e32 v8, v34, v8
	v_max_u32_e32 v34, v49, v5
	v_min_u32_e32 v5, v49, v5
	v_max_u32_e32 v49, v4, v21
	v_min_u32_e32 v4, v4, v21
	v_max_u32_e32 v21, v25, v10
	v_min_u32_e32 v10, v25, v10
	v_max_u32_e32 v25, v22, v29
	v_min_u32_e32 v22, v22, v29
	v_max_u32_e32 v29, v36, v30
	v_min_u32_e32 v30, v36, v30
	v_max_u32_e32 v36, v26, v39
	v_min_u32_e32 v26, v26, v39
	v_max_u32_e32 v38, v33, v11
	v_min_u32_e32 v11, v33, v11
	v_max_u32_e32 v33, v40, v35
	v_min_u32_e32 v35, v40, v35
	v_max_u32_e32 v40, v23, v7
	v_min_u32_e32 v7, v23, v7
	v_max_u32_e32 v23, v3, v6
	v_min_u32_e32 v3, v3, v6
	v_max_u32_e32 v6, v1, v2
	v_min_u32_e32 v1, v1, v2
	v_max_u32_e32 v2, v27, v0
	v_min_u32_e32 v0, v27, v0
	v_max_u32_e32 v27, v24, v32
	v_min_u32_e32 v24, v24, v32
	v_max_u32_e32 v32, v28, v31
	v_min_u32_e32 v28, v28, v31
	v_max_u32_e32 v39, v37, v34
	v_min_u32_e32 v34, v37, v34
	v_max_u32_e32 v37, v41, v49
	v_min_u32_e32 v41, v41, v49
	v_max_u32_e32 v49, v9, v5
	v_min_u32_e32 v5, v9, v5
	v_max_u32_e32 v9, v8, v4
	v_min_u32_e32 v4, v8, v4
	v_max_u32_e32 v8, v10, v30
	v_min_u32_e32 v10, v10, v30
	v_max_u32_e32 v30, v22, v26
	v_min_u32_e32 v22, v22, v26
	v_max_u32_e32 v26, v21, v29
	v_min_u32_e32 v21, v21, v29
	v_max_u32_e32 v29, v25, v36
	v_min_u32_e32 v25, v25, v36
	v_max_u32_e32 v31, v38, v33
	v_min_u32_e32 v33, v38, v33
	v_max_u32_e32 v38, v11, v35
	v_min_u32_e32 v11, v11, v35
	v_max_u32_e32 v35, v40, v23
	v_min_u32_e32 v23, v40, v23
	v_max_u32_e32 v40, v7, v3
	v_min_u32_e32 v3, v7, v3
	v_max_u32_e32 v7, v1, v0
	v_min_u32_e32 v0, v1, v0
	v_max_u32_e32 v1, v6, v2
	v_min_u32_e32 v2, v6, v2
	v_max_u32_e32 v6, v24, v28
	v_min_u32_e32 v24, v24, v28
	v_max_u32_e32 v28, v27, v32
	v_min_u32_e32 v27, v27, v32
	v_max_u32_e32 v36, v39, v37
	v_min_u32_e32 v37, v39, v37
	v_max_u32_e32 v39, v34, v41
	v_min_u32_e32 v34, v34, v41
	v_max_u32_e32 v41, v49, v9
	v_min_u32_e32 v9, v49, v9
	v_max_u32_e32 v49, v5, v4
	v_min_u32_e32 v4, v5, v4
	v_max_u32_e32 v5, v10, v22
	v_min_u32_e32 v10, v10, v22
	v_max_u32_e32 v22, v8, v30
	v_min_u32_e32 v8, v8, v30
	v_max_u32_e32 v30, v21, v25
	v_min_u32_e32 v21, v21, v25
	v_max_u32_e32 v25, v26, v29
	v_min_u32_e32 v26, v26, v29
	v_max_u32_e32 v32, v31, v0
	v_min_u32_e32 v0, v31, v0
	v_max_u32_e32 v31, v33, v7
	v_min_u32_e32 v7, v33, v7
	v_max_u32_e32 v33, v38, v2
	v_min_u32_e32 v2, v38, v2
	v_max_u32_e32 v38, v11, v1
	v_min_u32_e32 v1, v11, v1
	v_max_u32_e32 v11, v35, v24
	v_min_u32_e32 v24, v35, v24
	v_max_u32_e32 v35, v23, v6
	v_min_u32_e32 v6, v23, v6
	v_max_u32_e32 v23, v40, v27
	v_min_u32_e32 v27, v40, v27
	v_max_u32_e32 v40, v3, v28
	v_min_u32_e32 v3, v3, v28
	v_max_u32_e32 v29, v36, v10
	v_min_u32_e32 v10, v36, v10
	v_max_u32_e32 v36, v37, v5
	v_min_u32_e32 v5, v37, v5
	v_max_u32_e32 v37, v39, v8
	v_min_u32_e32 v8, v39, v8
	v_max_u32_e32 v39, v34, v22
	v_min_u32_e32 v22, v34, v22
	v_max_u32_e32 v34, v41, v21
	v_min_u32_e32 v21, v41, v21
	v_max_u32_e32 v41, v9, v30
	v_min_u32_e32 v9, v9, v30
	v_max_u32_e32 v30, v49, v26
	v_min_u32_e32 v26, v49, v26
	v_max_u32_e32 v49, v4, v25
	v_min_u32_e32 v4, v4, v25
	v_max_u32_e32 v28, v32, v11
	v_min_u32_e32 v11, v32, v11
	v_max_u32_e32 v32, v31, v35
	v_min_u32_e32 v31, v31, v35
	v_max_u32_e32 v35, v33, v23
	v_min_u32_e32 v23, v33, v23
	v_max_u32_e32 v33, v38, v40
	v_min_u32_e32 v38, v38, v40
	v_max_u32_e32 v40, v0, v24
	v_min_u32_e32 v0, v0, v24
	v_max_u32_e32 v24, v7, v6
	v_min_u32_e32 v6, v7, v6
	v_max_u32_e32 v7, v2, v27
	v_min_u32_e32 v2, v2, v27
	v_max_u32_e32 v27, v1, v3
	v_min_u32_e32 v1, v1, v3
	v_max_u32_e32 v25, v29, v34
	v_min_u32_e32 v29, v29, v34
	v_max_u32_e32 v34, v36, v41
	v_min_u32_e32 v36, v36, v41
	v_max_u32_e32 v41, v37, v30
	v_min_u32_e32 v30, v37, v30
	v_max_u32_e32 v37, v39, v49
	v_min_u32_e32 v39, v39, v49
	v_max_u32_e32 v49, v10, v21
	v_min_u32_e32 v10, v10, v21
	v_max_u32_e32 v21, v5, v9
	v_min_u32_e32 v5, v5, v9
	v_max_u32_e32 v9, v8, v26
	v_min_u32_e32 v8, v8, v26
	v_max_u32_e32 v26, v22, v4
	v_min_u32_e32 v4, v22, v4
	v_max_u32_e32 v3, v28, v35
	v_min_u32_e32 v28, v28, v35
	v_max_u32_e32 v35, v32, v33
	v_min_u32_e32 v32, v32, v33
	v_max_u32_e32 v33, v11, v23
	v_min_u32_e32 v11, v11, v23
	v_max_u32_e32 v23, v31, v38
	v_min_u32_e32 v31, v31, v38
	v_max_u32_e32 v38, v40, v7
	v_min_u32_e32 v7, v40, v7
	v_max_u32_e32 v40, v24, v27
	v_min_u32_e32 v24, v24, v27
	v_max_u32_e32 v27, v0, v2
	v_min_u32_e32 v0, v0, v2
	v_max_u32_e32 v2, v6, v1
	v_min_u32_e32 v1, v6, v1
	v_max_u32_e32 v22, v25, v41
	v_min_u32_e32 v25, v25, v41
	v_max_u32_e32 v41, v34, v37
	v_min_u32_e32 v34, v34, v37
	v_max_u32_e32 v37, v29, v30
	v_min_u32_e32 v29, v29, v30
	v_max_u32_e32 v30, v36, v39
	v_min_u32_e32 v36, v36, v39
	v_max_u32_e32 v39, v49, v9
	v_min_u32_e32 v9, v49, v9
	v_max_u32_e32 v49, v21, v26
	v_min_u32_e32 v21, v21, v26
	v_max_u32_e32 v26, v10, v8
	v_min_u32_e32 v8, v10, v8
	v_max_u32_e32 v10, v5, v4
	v_min_u32_e32 v4, v5, v4
	v_min_u32_e32 v6, v3, v35
	v_min_u32_e32 v42, v28, v32
	v_min_u32_e32 v43, v33, v23
	v_min_u32_e32 v44, v11, v31
	v_min_u32_e32 v45, v38, v40
	v_min_u32_e32 v46, v7, v24
	v_min_u32_e32 v47, v27, v2
	v_min_u32_e32 v48, v0, v1
	v_min_u32_e32 v5, v22, v41
	v_min_u32_e32 v50, v25, v34
	v_min_u32_e32 v51, v37, v30
	v_min_u32_e32 v52, v29, v36
	v_min_u32_e32 v53, v39, v49
	v_min_u32_e32 v54, v9, v21
	v_min_u32_e32 v55, v26, v10
	v_min_u32_e32 v56, v8, v4
	v_max3_u32 v3, v3, v35, v56
	v_max3_u32 v4, v6, v8, v4
	v_max3_u32 v6, v28, v32, v55
	v_max3_u32 v8, v42, v26, v10
	v_max3_u32 v10, v33, v23, v54
	v_max3_u32 v9, v43, v9, v21
	v_max3_u32 v11, v11, v31, v53
	v_max3_u32 v21, v44, v39, v49
	v_max3_u32 v23, v38, v40, v52
	v_max3_u32 v26, v45, v29, v36
	v_max3_u32 v7, v7, v24, v51
	v_max3_u32 v24, v46, v37, v30
	v_max3_u32 v2, v27, v2, v50
	v_max3_u32 v25, v47, v25, v34
	v_max3_u32 v0, v0, v1, v5
	v_max3_u32 v1, v48, v22, v41
	v_max_u32_e32 v5, v3, v23
	v_min_u32_e32 v3, v3, v23
	v_max_u32_e32 v22, v4, v26
	v_min_u32_e32 v4, v4, v26
	v_max_u32_e32 v23, v6, v7
	v_min_u32_e32 v6, v6, v7
	v_max_u32_e32 v7, v8, v24
	v_min_u32_e32 v8, v8, v24
	v_max_u32_e32 v24, v10, v2
	v_min_u32_e32 v2, v10, v2
	v_max_u32_e32 v10, v9, v25
	v_min_u32_e32 v9, v9, v25
	v_max_u32_e32 v25, v11, v0
	v_min_u32_e32 v0, v11, v0
	v_max_u32_e32 v11, v21, v1
	v_min_u32_e32 v1, v21, v1
	v_max_u32_e32 v21, v5, v24
	v_min_u32_e32 v5, v5, v24
	v_max_u32_e32 v24, v22, v10
	v_min_u32_e32 v10, v22, v10
	v_max_u32_e32 v22, v23, v25
	v_min_u32_e32 v23, v23, v25
	v_max_u32_e32 v25, v7, v11
	v_min_u32_e32 v7, v7, v11
	v_max_u32_e32 v11, v3, v2
	v_min_u32_e32 v2, v3, v2
	v_max_u32_e32 v3, v4, v9
	v_min_u32_e32 v4, v4, v9
	v_max_u32_e32 v9, v6, v0
	v_min_u32_e32 v0, v6, v0
	v_max_u32_e32 v6, v8, v1
	v_min_u32_e32 v1, v8, v1
	v_max_u32_e32 v8, v21, v22
	v_min_u32_e32 v21, v21, v22
	v_max_u32_e32 v22, v24, v25
	v_min_u32_e32 v24, v24, v25
	v_max_u32_e32 v25, v5, v23
	v_min_u32_e32 v5, v5, v23
	v_max_u32_e32 v23, v10, v7
	v_min_u32_e32 v7, v10, v7
	v_max_u32_e32 v10, v11, v9
	v_min_u32_e32 v9, v11, v9
	v_max_u32_e32 v11, v3, v6
	v_min_u32_e32 v3, v3, v6
	v_max_u32_e32 v6, v2, v0
	v_min_u32_e32 v0, v2, v0
	v_max_u32_e32 v2, v4, v1
	v_min_u32_e32 v1, v4, v1
	v_mov_b32_e32 v43, s53
	v_max_u32_e32 v41, v0, v1
	v_min_u32_e32 v42, v0, v1
	v_bitop3_b32 v1, v20, s18, v43 bitop3:0x36
	v_max_u32_e32 v28, v8, v22
	v_min_u32_e32 v29, v8, v22
	v_lshl_add_u32 v0, v20, 2, v18
	v_lshl_add_u32 v1, v1, 2, v12
	v_max_u32_e32 v30, v21, v24
	v_min_u32_e32 v21, v21, v24
	v_max_u32_e32 v31, v25, v23
	v_min_u32_e32 v32, v25, v23
	v_max_u32_e32 v33, v5, v7
	v_min_u32_e32 v34, v5, v7
	v_max_u32_e32 v35, v10, v11
	v_min_u32_e32 v36, v10, v11
	v_max_u32_e32 v37, v9, v3
	v_min_u32_e32 v38, v9, v3
	v_max_u32_e32 v39, v6, v2
	v_min_u32_e32 v40, v6, v2
	ds_write2st64_b32 v0, v28, v29 offset1:1
	ds_write2st64_b32 v0, v30, v21 offset0:2 offset1:3
	ds_write2st64_b32 v0, v31, v32 offset0:4 offset1:5
	ds_write2st64_b32 v0, v33, v34 offset0:6 offset1:7
	ds_write2st64_b32 v0, v35, v36 offset0:8 offset1:9
	ds_write2st64_b32 v0, v37, v38 offset0:10 offset1:11
	ds_write2st64_b32 v0, v39, v40 offset0:12 offset1:13
	ds_write2st64_b32 v0, v41, v42 offset0:14 offset1:15
	s_waitcnt lgkmcnt(0)
	s_barrier
	ds_read2st64_b32 v[2:3], v1 offset1:1
	ds_read2st64_b32 v[4:5], v1 offset0:2 offset1:3
	ds_read2st64_b32 v[6:7], v1 offset0:4 offset1:5
	ds_read2st64_b32 v[8:9], v1 offset0:6 offset1:7
	ds_read2st64_b32 v[10:11], v1 offset0:8 offset1:9
	ds_read2st64_b32 v[22:23], v1 offset0:10 offset1:11
	ds_read2st64_b32 v[24:25], v1 offset0:12 offset1:13
	ds_read2st64_b32 v[26:27], v1 offset0:14 offset1:15
	s_waitcnt lgkmcnt(4)
	v_max_u32_e32 v9, v35, v9
	s_waitcnt lgkmcnt(3)
	v_max_u32_e32 v11, v33, v11
	s_waitcnt lgkmcnt(2)
	v_max_u32_e32 v23, v31, v23
	s_waitcnt lgkmcnt(1)
	v_max_u32_e32 v25, v30, v25
	s_waitcnt lgkmcnt(0)
	v_max_u32_e32 v27, v28, v27
	v_max_u32_e32 v26, v29, v26
	v_max_u32_e32 v21, v21, v24
	v_max_u32_e32 v22, v32, v22
	v_max_u32_e32 v10, v34, v10
	v_max_u32_e32 v8, v36, v8
	v_max_u32_e32 v7, v37, v7
	v_max_u32_e32 v6, v38, v6
	v_max_u32_e32 v5, v39, v5
	v_max_u32_e32 v4, v40, v4
	v_max_u32_e32 v3, v41, v3
	v_max_u32_e32 v2, v42, v2
	v_max_u32_e32 v24, v27, v9
	v_min_u32_e32 v9, v27, v9
	v_max_u32_e32 v27, v26, v8
	v_min_u32_e32 v8, v26, v8
	v_max_u32_e32 v26, v25, v7
	v_min_u32_e32 v7, v25, v7
	v_max_u32_e32 v25, v21, v6
	v_min_u32_e32 v6, v21, v6
	v_max_u32_e32 v21, v23, v5
	v_min_u32_e32 v5, v23, v5
	v_max_u32_e32 v23, v22, v4
	v_min_u32_e32 v4, v22, v4
	v_max_u32_e32 v22, v11, v3
	v_min_u32_e32 v3, v11, v3
	v_max_u32_e32 v11, v10, v2
	v_min_u32_e32 v2, v10, v2
	v_max_u32_e32 v10, v24, v21
	v_min_u32_e32 v21, v24, v21
	v_max_u32_e32 v24, v27, v23
	v_min_u32_e32 v23, v27, v23
	v_max_u32_e32 v27, v26, v22
	v_min_u32_e32 v22, v26, v22
	v_max_u32_e32 v26, v25, v11
	v_min_u32_e32 v11, v25, v11
	v_max_u32_e32 v25, v9, v5
	v_min_u32_e32 v5, v9, v5
	v_max_u32_e32 v9, v8, v4
	v_min_u32_e32 v4, v8, v4
	v_max_u32_e32 v8, v7, v3
	v_min_u32_e32 v3, v7, v3
	v_max_u32_e32 v7, v6, v2
	v_min_u32_e32 v2, v6, v2
	v_max_u32_e32 v6, v10, v27
	v_min_u32_e32 v10, v10, v27
	v_max_u32_e32 v27, v24, v26
	v_min_u32_e32 v24, v24, v26
	v_max_u32_e32 v28, v21, v22
	v_min_u32_e32 v22, v21, v22
	v_max_u32_e32 v21, v23, v11
	v_min_u32_e32 v29, v23, v11
	v_max_u32_e32 v30, v25, v8
	v_min_u32_e32 v8, v25, v8
	v_max_u32_e32 v25, v9, v7
	v_min_u32_e32 v7, v9, v7
	v_min_u32_e32 v32, v5, v3
	v_max_u32_e32 v33, v4, v2
	v_min_u32_e32 v2, v4, v2
	s_movk_i32 s18, 0x1000
	v_max_u32_e32 v31, v5, v3
	v_max_u32_e32 v26, v6, v27
	v_min_u32_e32 v5, v6, v27
	v_max_u32_e32 v11, v10, v24
	v_min_u32_e32 v3, v10, v24
	v_max_u32_e32 v23, v28, v21
	v_min_u32_e32 v6, v28, v21
	v_max_u32_e32 v21, v22, v29
	v_min_u32_e32 v4, v22, v29
	v_max_u32_e32 v22, v8, v7
	v_min_u32_e32 v7, v8, v7
	v_max_u32_e32 v24, v32, v2
	v_min_u32_e32 v8, v32, v2
	v_bitop3_b32 v2, v20, s18, v43 bitop3:0x36
	v_max_u32_e32 v27, v30, v25
	v_min_u32_e32 v9, v30, v25
	v_max_u32_e32 v25, v31, v33
	v_min_u32_e32 v10, v31, v33
	v_lshl_add_u32 v2, v2, 2, v12
	s_and_b64 vcc, exec, s[58:59]
	ds_write2st64_b32 v0, v26, v5 offset0:132 offset1:133
	ds_write2st64_b32 v0, v11, v3 offset0:134 offset1:135
	ds_write2st64_b32 v0, v23, v6 offset0:136 offset1:137
	ds_write2st64_b32 v0, v21, v4 offset0:138 offset1:139
	ds_write2st64_b32 v0, v27, v9 offset0:140 offset1:141
	ds_write2st64_b32 v0, v22, v7 offset0:142 offset1:143
	ds_write2st64_b32 v0, v25, v10 offset0:144 offset1:145
	ds_write2st64_b32 v0, v24, v8 offset0:146 offset1:147
	s_waitcnt lgkmcnt(0)
	s_barrier
	s_cbranch_vccz .LBB0_1038
	ds_read2st64_b32 v[28:29], v2 offset0:146 offset1:147
	ds_read2st64_b32 v[30:31], v2 offset0:138 offset1:139
	ds_read2st64_b32 v[32:33], v2 offset0:142 offset1:143
	ds_read2st64_b32 v[34:35], v2 offset0:144 offset1:145
	ds_read2st64_b32 v[36:37], v2 offset0:134 offset1:135
	ds_read2st64_b32 v[38:39], v2 offset0:136 offset1:137
	s_waitcnt lgkmcnt(5)
	v_max_u32_e32 v29, v26, v29
	s_waitcnt lgkmcnt(4)
	v_max_u32_e32 v31, v27, v31
	ds_read2st64_b32 v[26:27], v2 offset0:140 offset1:141
	ds_read2st64_b32 v[40:41], v2 offset0:132 offset1:133
	s_waitcnt lgkmcnt(5)
	v_max_u32_e32 v23, v23, v33
	s_waitcnt lgkmcnt(3)
	v_max_u32_e32 v25, v25, v37
	v_max_u32_e32 v11, v11, v35
	s_waitcnt lgkmcnt(2)
	v_max_u32_e32 v22, v22, v39
	s_waitcnt lgkmcnt(1)
	v_max_u32_e32 v21, v21, v27
	s_waitcnt lgkmcnt(0)
	v_max_u32_e32 v24, v24, v41
	v_max_u32_e32 v5, v5, v28
	v_max_u32_e32 v9, v9, v30
	v_max_u32_e32 v6, v6, v32
	v_max_u32_e32 v10, v10, v36
	v_max_u32_e32 v3, v3, v34
	v_max_u32_e32 v7, v7, v38
	v_max_u32_e32 v4, v4, v26
	v_max_u32_e32 v8, v8, v40
	v_min_u32_e32 v42, v29, v31
	v_min_u32_e32 v33, v23, v25
	v_min_u32_e32 v35, v11, v22
	v_min_u32_e32 v27, v21, v24
	v_min_u32_e32 v28, v5, v9
	v_min_u32_e32 v30, v6, v10
	v_min_u32_e32 v34, v3, v7
	v_min_u32_e32 v26, v4, v8
	v_min_u32_e32 v37, v42, v33
	v_min_u32_e32 v39, v35, v27
	v_min_u32_e32 v32, v28, v30
	v_min_u32_e32 v36, v34, v26
	v_max_u32_e32 v33, v42, v33
	v_max_u32_e32 v27, v35, v27
	v_max_u32_e32 v28, v28, v30
	v_max_u32_e32 v26, v34, v26
	v_min_u32_e32 v35, v33, v27
	v_min_u32_e32 v30, v28, v26
	v_max_u32_e32 v27, v33, v27
	v_max_u32_e32 v26, v28, v26
	v_min_u32_e32 v28, v27, v26
	v_max_u32_e32 v26, v27, v26
	v_max_u32_e32 v27, v29, v31
	v_max_u32_e32 v23, v23, v25
	v_max_u32_e32 v11, v11, v22
	v_max_u32_e32 v21, v21, v24
	v_max_u32_e32 v5, v5, v9
	v_max_u32_e32 v6, v6, v10
	v_max_u32_e32 v3, v3, v7
	v_max_u32_e32 v4, v4, v8
	v_min_u32_e32 v25, v27, v23
	v_min_u32_e32 v22, v11, v21
	v_min_u32_e32 v9, v5, v6
	v_min_u32_e32 v7, v3, v4
	v_min_u32_e32 v24, v25, v22
	v_min_u32_e32 v8, v9, v7
	v_max_u32_e32 v22, v25, v22
	v_max_u32_e32 v7, v9, v7
	v_min_u32_e32 v9, v22, v7
	v_max_u32_e32 v7, v22, v7
	v_max_u32_e32 v22, v27, v23
	v_max_u32_e32 v11, v11, v21
	v_max_u32_e32 v5, v5, v6
	v_max_u32_e32 v3, v3, v4
	v_min_u32_e32 v21, v22, v11
	v_min_u32_e32 v4, v5, v3
	v_max_u32_e32 v11, v22, v11
	v_max_u32_e32 v3, v5, v3
	v_min_u32_e32 v41, v37, v39
	v_min_u32_e32 v38, v32, v36
	v_max_u32_e32 v37, v37, v39
	v_max_u32_e32 v32, v32, v36
	v_min_u32_e32 v5, v11, v3
	v_max_u32_e32 v3, v11, v3
	v_lshl_add_u32 v11, v20, 2, v19
	v_min_u32_e32 v40, v41, v38
	v_max_u32_e32 v38, v41, v38
	v_min_u32_e32 v36, v37, v32
	v_max_u32_e32 v32, v37, v32
	v_min_u32_e32 v34, v35, v30
	v_max_u32_e32 v30, v35, v30
	v_min_u32_e32 v10, v24, v8
	v_max_u32_e32 v8, v24, v8
	v_min_u32_e32 v6, v21, v4
	v_max_u32_e32 v4, v21, v4
	ds_write2st64_b32 v11, v3, v5 offset1:1
	ds_write2st64_b32 v11, v4, v6 offset0:2 offset1:3
	ds_write2st64_b32 v11, v7, v9 offset0:4 offset1:5
	ds_write2st64_b32 v11, v8, v10 offset0:6 offset1:7
	ds_write2st64_b32 v11, v26, v28 offset0:8 offset1:9
	ds_write2st64_b32 v11, v30, v34 offset0:10 offset1:11
	ds_write2st64_b32 v11, v32, v36 offset0:12 offset1:13
	ds_write2st64_b32 v11, v38, v40 offset0:14 offset1:15
